# fp8 GEMM K-loops: s_nop 3 instead of s_nop 1 in front of each 16x16x128 MFMA (issue spacing)
# baseline (speedup 1.0000x reference)
.LBB0_239:
	s_add_u32 s3, s10, 0xfffe0080
	s_addc_u32 s30, s11, -1
	s_add_i32 s2, 0, 0x10000
	s_cmp_eq_u32 s56, 4
	s_cselect_b32 s35, s9, s30
	s_cselect_b32 s34, s23, s3
	v_add_u32_e32 v1, s2, v19
	s_cselect_b32 s31, s21, s55
	s_cselect_b32 s30, s29, s54
	s_add_i32 s3, 0, 0x14000
	ds_read_b128 v[28:31], v1
	ds_read_b128 v[32:35], v1 offset:1024
	ds_read_b128 v[36:39], v1 offset:2048
	ds_read_b128 v[40:43], v1 offset:3072
	v_add_u32_e32 v1, s3, v19
	s_waitcnt lgkmcnt(0)
	ds_read_b128 v[4:7], v1
	ds_read_b128 v[8:11], v1 offset:1024
	ds_read_b128 v[20:23], v1 offset:2048
	ds_read_b128 v[24:27], v1 offset:3072
	v_lshl_add_u64 v[200:201], s[10:11], 0, v[170:171]
	s_add_i32 m0, s43, 0xc000
	ds_read_b128 v[174:177], v182
	ds_read_b128 v[178:181], v182 offset:1024
	ds_read_b128 v[184:187], v182 offset:2048
	ds_read_b128 v[188:191], v182 offset:3072
	ds_read_b128 v[192:195], v182 offset:4096
	ds_read_b128 v[196:199], v182 offset:5120
	ds_read_b128 v[204:207], v182 offset:6144
	ds_read_b128 v[208:211], v182 offset:7168
	global_load_lds_dwordx4 v[200:201], off
	v_lshl_add_u64 v[200:201], s[10:11], 0, v[172:173]
	s_add_i32 m0, s43, 0xe000
	s_nop 0
	global_load_lds_dwordx4 v[200:201], off
	s_waitcnt vmcnt(8)
	s_waitcnt lgkmcnt(0)
	s_barrier
	s_setprio 1
	s_waitcnt lgkmcnt(0)
	s_nop 3
	v_mfma_f32_16x16x128_f8f6f4 v[164:167], v[28:35], v[174:181], v[164:167]
	s_nop 3
	v_mfma_f32_16x16x128_f8f6f4 v[160:163], v[36:43], v[174:181], v[160:163]
	s_nop 3
	v_mfma_f32_16x16x128_f8f6f4 v[148:151], v[28:35], v[184:191], v[148:151]
	s_nop 3
	v_mfma_f32_16x16x128_f8f6f4 v[144:147], v[36:43], v[184:191], v[144:147]
	s_nop 3
	v_mfma_f32_16x16x128_f8f6f4 v[132:135], v[28:35], v[192:199], v[132:135]
	s_nop 3
	v_mfma_f32_16x16x128_f8f6f4 v[128:131], v[36:43], v[192:199], v[128:131]
	s_nop 3
	v_mfma_f32_16x16x128_f8f6f4 v[116:119], v[28:35], v[204:211], v[116:119]
	s_nop 3
	v_mfma_f32_16x16x128_f8f6f4 v[112:115], v[36:43], v[204:211], v[112:115]
	s_setprio 0
	s_setprio 1
	s_nop 3
	v_mfma_f32_16x16x128_f8f6f4 v[156:159], v[4:11], v[174:181], v[156:159]
	s_nop 3
	v_mfma_f32_16x16x128_f8f6f4 v[152:155], v[20:27], v[174:181], v[152:155]
	s_nop 3
	v_mfma_f32_16x16x128_f8f6f4 v[140:143], v[4:11], v[184:191], v[140:143]
	s_nop 3
	v_mfma_f32_16x16x128_f8f6f4 v[136:139], v[20:27], v[184:191], v[136:139]
	s_nop 3
	v_mfma_f32_16x16x128_f8f6f4 v[124:127], v[4:11], v[192:199], v[124:127]
	s_nop 3
	v_mfma_f32_16x16x128_f8f6f4 v[120:123], v[20:27], v[192:199], v[120:123]
	s_nop 3
	v_mfma_f32_16x16x128_f8f6f4 v[108:111], v[4:11], v[204:211], v[108:111]
	s_nop 3
	v_mfma_f32_16x16x128_f8f6f4 v[104:107], v[20:27], v[204:211], v[104:107]
	s_setprio 0
	s_barrier
	s_add_i32 s2, s2, s42
	v_lshl_add_u64 v[174:175], s[30:31], 0, v[16:17]
	s_mov_b32 m0, s2
	ds_read_b128 v[184:187], v182 offset:16384
	ds_read_b128 v[188:191], v182 offset:17408
	ds_read_b128 v[192:195], v182 offset:18432
	ds_read_b128 v[196:199], v182 offset:19456
	ds_read_b128 v[204:207], v182 offset:20480
	ds_read_b128 v[208:211], v182 offset:21504
	ds_read_b128 v[230:233], v182 offset:22528
	ds_read_b128 v[234:237], v182 offset:23552
	global_load_lds_dwordx4 v[174:175], off
	s_add_i32 m0, s2, 0x2000
	s_add_u32 s58, s30, 0x20000
	v_lshl_add_u64 v[176:177], s[30:31], 0, v[168:169]
	s_addc_u32 s59, s31, 0
	s_add_i32 s2, s3, s42
	global_load_lds_dwordx4 v[176:177], off
	v_lshl_add_u64 v[178:179], s[58:59], 0, v[16:17]
	s_mov_b32 m0, s2
	v_lshl_add_u64 v[180:181], s[34:35], 0, v[168:169]
	global_load_lds_dwordx4 v[178:179], off
	v_lshl_add_u64 v[178:179], s[58:59], 0, v[168:169]
	s_add_i32 m0, s2, 0x2000
	s_nop 0
	global_load_lds_dwordx4 v[178:179], off
	v_lshl_add_u64 v[178:179], s[34:35], 0, v[16:17]
	s_mov_b32 m0, s43
	s_nop 0
	global_load_lds_dwordx4 v[178:179], off
	s_mov_b32 m0, s44
	s_nop 0
	global_load_lds_dwordx4 v[180:181], off
	s_waitcnt vmcnt(8)
	s_waitcnt lgkmcnt(0)
	s_barrier
	s_setprio 1
	s_waitcnt lgkmcnt(0)
	s_nop 3
	v_mfma_f32_16x16x128_f8f6f4 v[100:103], v[28:35], v[184:191], v[100:103]
	s_nop 3
	v_mfma_f32_16x16x128_f8f6f4 v[96:99], v[36:43], v[184:191], v[96:99]
	s_nop 3
	v_mfma_f32_16x16x128_f8f6f4 v[84:87], v[28:35], v[192:199], v[84:87]
	s_nop 3
	v_mfma_f32_16x16x128_f8f6f4 v[80:83], v[36:43], v[192:199], v[80:83]
	s_nop 3
	v_mfma_f32_16x16x128_f8f6f4 v[68:71], v[28:35], v[204:211], v[68:71]
	s_nop 3
	v_mfma_f32_16x16x128_f8f6f4 v[64:67], v[36:43], v[204:211], v[64:67]
	s_nop 3
	v_mfma_f32_16x16x128_f8f6f4 v[52:55], v[28:35], v[230:237], v[52:55]
	s_nop 3
	v_mfma_f32_16x16x128_f8f6f4 v[48:51], v[36:43], v[230:237], v[48:51]
	s_setprio 0
	s_setprio 1
	s_nop 3
	v_mfma_f32_16x16x128_f8f6f4 v[92:95], v[4:11], v[184:191], v[92:95]
	s_nop 3
	v_mfma_f32_16x16x128_f8f6f4 v[88:91], v[20:27], v[184:191], v[88:91]
	s_nop 3
	v_mfma_f32_16x16x128_f8f6f4 v[76:79], v[4:11], v[192:199], v[76:79]
	s_nop 3
	v_mfma_f32_16x16x128_f8f6f4 v[72:75], v[20:27], v[192:199], v[72:75]
	s_nop 3
	v_mfma_f32_16x16x128_f8f6f4 v[60:63], v[4:11], v[204:211], v[60:63]
	s_nop 3
	v_mfma_f32_16x16x128_f8f6f4 v[56:59], v[20:27], v[204:211], v[56:59]
	s_nop 3
	v_mfma_f32_16x16x128_f8f6f4 v[44:47], v[4:11], v[230:237], v[44:47]
	s_nop 3
	v_mfma_f32_16x16x128_f8f6f4 v[12:15], v[20:27], v[230:237], v[12:15]
	s_setprio 0
	s_barrier
	s_add_i32 s33, 0, 0x18000
	v_add_u32_e32 v1, s33, v19
	s_add_i32 s57, 0, 0x1c000
	ds_read_b128 v[4:7], v1
	ds_read_b128 v[8:11], v1 offset:1024
	ds_read_b128 v[20:23], v1 offset:2048
	ds_read_b128 v[24:27], v1 offset:3072
	v_add_u32_e32 v1, s57, v19
	ds_read_b128 v[28:31], v1
	ds_read_b128 v[32:35], v1 offset:1024
	ds_read_b128 v[36:39], v1 offset:2048
	ds_read_b128 v[40:43], v1 offset:3072
	s_add_u32 s2, s34, 0x20000
	s_addc_u32 s3, s35, 0
	s_mov_b32 m0, s45
	v_lshl_add_u64 v[200:201], s[2:3], 0, v[16:17]
	ds_read_b128 v[184:187], v182 offset:32768
	ds_read_b128 v[188:191], v182 offset:33792
	ds_read_b128 v[192:195], v182 offset:34816
	ds_read_b128 v[196:199], v182 offset:35840
	ds_read_b128 v[204:207], v182 offset:36864
	ds_read_b128 v[208:211], v182 offset:37888
	ds_read_b128 v[230:233], v182 offset:38912
	ds_read_b128 v[234:237], v182 offset:39936
	global_load_lds_dwordx4 v[200:201], off
	v_lshl_add_u64 v[200:201], s[2:3], 0, v[168:169]
	s_mov_b32 m0, s46
	s_nop 0
	global_load_lds_dwordx4 v[200:201], off
	s_waitcnt vmcnt(8)
	s_waitcnt lgkmcnt(0)
	s_barrier
	s_setprio 1
	s_waitcnt lgkmcnt(0)
	s_nop 3
	v_mfma_f32_16x16x128_f8f6f4 v[164:167], v[4:11], v[184:191], v[164:167]
	s_nop 3
	v_mfma_f32_16x16x128_f8f6f4 v[160:163], v[20:27], v[184:191], v[160:163]
	s_nop 3
	v_mfma_f32_16x16x128_f8f6f4 v[148:151], v[4:11], v[192:199], v[148:151]
	s_nop 3
	v_mfma_f32_16x16x128_f8f6f4 v[144:147], v[20:27], v[192:199], v[144:147]
	s_nop 3
	v_mfma_f32_16x16x128_f8f6f4 v[132:135], v[4:11], v[204:211], v[132:135]
	s_nop 3
	v_mfma_f32_16x16x128_f8f6f4 v[128:131], v[20:27], v[204:211], v[128:131]
	s_nop 3
	v_mfma_f32_16x16x128_f8f6f4 v[116:119], v[4:11], v[230:237], v[116:119]
	s_nop 3
	v_mfma_f32_16x16x128_f8f6f4 v[112:115], v[20:27], v[230:237], v[112:115]
	s_setprio 0
	s_setprio 1
	s_nop 3
	v_mfma_f32_16x16x128_f8f6f4 v[156:159], v[28:35], v[184:191], v[156:159]
	s_nop 3
	v_mfma_f32_16x16x128_f8f6f4 v[152:155], v[36:43], v[184:191], v[152:155]
	s_nop 3
	v_mfma_f32_16x16x128_f8f6f4 v[140:143], v[28:35], v[192:199], v[140:143]
	s_nop 3
	v_mfma_f32_16x16x128_f8f6f4 v[136:139], v[36:43], v[192:199], v[136:139]
	s_nop 3
	v_mfma_f32_16x16x128_f8f6f4 v[124:127], v[28:35], v[204:211], v[124:127]
	s_nop 3
	v_mfma_f32_16x16x128_f8f6f4 v[120:123], v[36:43], v[204:211], v[120:123]
	s_nop 3
	v_mfma_f32_16x16x128_f8f6f4 v[108:111], v[28:35], v[230:237], v[108:111]
	s_nop 3
	v_mfma_f32_16x16x128_f8f6f4 v[104:107], v[36:43], v[230:237], v[104:107]
	s_setprio 0
	s_barrier
	s_add_i32 s2, s33, s42
	v_lshl_add_u64 v[174:175], v[174:175], 0, s[86:87]
	s_mov_b32 m0, s2
	ds_read_b128 v[184:187], v182 offset:49152
	ds_read_b128 v[188:191], v182 offset:50176
	ds_read_b128 v[192:195], v182 offset:51200
	ds_read_b128 v[196:199], v182 offset:52224
	ds_read_b128 v[204:207], v182 offset:53248
	ds_read_b128 v[208:211], v182 offset:54272
	ds_read_b128 v[230:233], v182 offset:55296
	ds_read_b128 v[234:237], v182 offset:56320
	global_load_lds_dwordx4 v[174:175], off
	s_add_i32 m0, s2, 0x2000
	s_add_u32 s2, s30, 0x20080
	v_lshl_add_u64 v[174:175], v[176:177], 0, s[86:87]
	s_addc_u32 s3, s31, 0
	s_add_i32 s30, s57, s42
	global_load_lds_dwordx4 v[174:175], off
	v_lshl_add_u64 v[174:175], s[2:3], 0, v[16:17]
	s_mov_b32 m0, s30
	s_nop 0
	global_load_lds_dwordx4 v[174:175], off
	v_lshl_add_u64 v[174:175], s[2:3], 0, v[168:169]
	s_add_i32 m0, s30, 0x2000
	s_nop 0
	global_load_lds_dwordx4 v[174:175], off
	v_lshl_add_u64 v[174:175], v[178:179], 0, s[86:87]
	s_mov_b32 m0, s49
	s_nop 0
	global_load_lds_dwordx4 v[174:175], off
	v_lshl_add_u64 v[174:175], v[180:181], 0, s[86:87]
	s_mov_b32 m0, s50
	s_nop 0
	global_load_lds_dwordx4 v[174:175], off
	s_waitcnt vmcnt(8)
	s_waitcnt lgkmcnt(0)
	s_barrier
	s_setprio 1
	s_waitcnt lgkmcnt(0)
	s_nop 3
	v_mfma_f32_16x16x128_f8f6f4 v[100:103], v[4:11], v[184:191], v[100:103]
	s_nop 3
	v_mfma_f32_16x16x128_f8f6f4 v[96:99], v[20:27], v[184:191], v[96:99]
	s_nop 3
	v_mfma_f32_16x16x128_f8f6f4 v[84:87], v[4:11], v[192:199], v[84:87]
	s_nop 3
	v_mfma_f32_16x16x128_f8f6f4 v[80:83], v[20:27], v[192:199], v[80:83]
	s_nop 3
	v_mfma_f32_16x16x128_f8f6f4 v[68:71], v[4:11], v[204:211], v[68:71]
	s_nop 3
	v_mfma_f32_16x16x128_f8f6f4 v[64:67], v[20:27], v[204:211], v[64:67]
	s_nop 3
	v_mfma_f32_16x16x128_f8f6f4 v[52:55], v[4:11], v[230:237], v[52:55]
	s_nop 3
	v_mfma_f32_16x16x128_f8f6f4 v[48:51], v[20:27], v[230:237], v[48:51]
	s_setprio 0
	s_setprio 1
	s_nop 3
	v_mfma_f32_16x16x128_f8f6f4 v[92:95], v[28:35], v[184:191], v[92:95]
	s_nop 3
	v_mfma_f32_16x16x128_f8f6f4 v[88:91], v[36:43], v[184:191], v[88:91]
	s_nop 3
	v_mfma_f32_16x16x128_f8f6f4 v[76:79], v[28:35], v[192:199], v[76:79]
	s_nop 3
	v_mfma_f32_16x16x128_f8f6f4 v[72:75], v[36:43], v[192:199], v[72:75]
	s_nop 3
	v_mfma_f32_16x16x128_f8f6f4 v[60:63], v[28:35], v[204:211], v[60:63]
	s_nop 3
	v_mfma_f32_16x16x128_f8f6f4 v[56:59], v[36:43], v[204:211], v[56:59]
	s_nop 3
	v_mfma_f32_16x16x128_f8f6f4 v[44:47], v[28:35], v[230:237], v[44:47]
	s_nop 3
	v_mfma_f32_16x16x128_f8f6f4 v[12:15], v[36:43], v[230:237], v[12:15]
	s_setprio 0
	s_barrier
	s_add_i32 s56, s56, 2
	s_add_u32 s10, s10, 0x100
	s_addc_u32 s11, s11, 0
	s_add_u32 s54, s54, 0x100
	s_addc_u32 s55, s55, 0
	s_cmp_gt_u32 s56, 5
	s_cbranch_scc0 .LBB0_239
	s_and_b64 vcc, exec, s[18:19]
	s_cbranch_vccz .LBB0_242
	s_barrier

.LBB0_489:
	s_ashr_i32 s19, s18, 31
	s_lshl_b64 s[2:3], s[18:19], 18
	s_add_u32 s20, s37, s2
	s_addc_u32 s21, s38, s3
	s_and_b64 s[2:3], s[6:7], exec
	s_cselect_b32 s29, s21, s27
	s_cselect_b32 s28, s20, s26
	s_ashr_i32 s17, s16, 31
	s_lshl_b64 s[2:3], s[16:17], 16
	s_add_u32 s22, s39, s2
	s_addc_u32 s23, s40, s3
	s_add_u32 s34, s26, 0x20080
	s_addc_u32 s35, s27, 0
	s_add_u32 s26, s28, 0x20000
	s_addc_u32 s27, s29, 0
	s_add_i32 s17, 0, 0x10000
	s_and_b64 s[2:3], s[6:7], exec
	s_cselect_b32 s24, s22, s24
	s_cselect_b32 s25, s23, s25
	s_add_u32 s30, s24, 0x8000
	v_add_u32_e32 v1, s17, v19
	s_addc_u32 s31, s25, 0
	s_add_i32 s2, 0, 0x14000
	ds_read_b128 v[20:23], v1
	ds_read_b128 v[24:27], v1 offset:1024
	ds_read_b128 v[40:43], v1 offset:2048
	ds_read_b128 v[44:47], v1 offset:3072
	v_add_u32_e32 v1, s2, v19
	ds_read_b128 v[148:151], v1
	ds_read_b128 v[152:155], v1 offset:1024
	ds_read_b128 v[156:159], v1 offset:2048
	ds_read_b128 v[160:163], v1 offset:3072
	v_lshl_add_u64 v[4:5], s[34:35], 0, v[16:17]
	s_add_i32 m0, s42, 0xc000
	ds_read_b128 v[8:11], v146
	ds_read_b128 v[12:15], v146 offset:1024
	ds_read_b128 v[28:31], v146 offset:2048
	ds_read_b128 v[32:35], v146 offset:3072
	ds_read_b128 v[48:51], v146 offset:4096
	ds_read_b128 v[52:55], v146 offset:5120
	ds_read_b128 v[56:59], v146 offset:6144
	ds_read_b128 v[60:63], v146 offset:7168
	global_load_lds_dwordx4 v[4:5], off
	v_lshl_add_u64 v[4:5], s[34:35], 0, v[136:137]
	s_add_i32 m0, s42, 0xe000
	s_nop 0
	global_load_lds_dwordx4 v[4:5], off
	s_waitcnt vmcnt(8)
	s_waitcnt lgkmcnt(0)
	s_barrier
	s_setprio 1
	v_readlane_b32 s52, v254, 22
	v_readlane_b32 s53, v254, 23
	v_readlane_b32 s54, v254, 24
	v_readlane_b32 s55, v254, 25
	v_mov_b64_e32 v[4:5], s[52:53]
	s_nop 0
	v_mov_b64_e32 v[130:131], s[54:55]
	v_mov_b64_e32 v[134:135], s[54:55]
	v_mov_b64_e32 v[114:115], s[54:55]
	v_mov_b64_e32 v[118:119], s[54:55]
	v_mov_b64_e32 v[98:99], s[54:55]
	v_mov_b64_e32 v[102:103], s[54:55]
	v_mov_b64_e32 v[82:83], s[54:55]
	v_mov_b64_e32 v[86:87], s[54:55]
	v_mov_b64_e32 v[6:7], s[54:55]
	v_mov_b64_e32 v[128:129], s[52:53]
	v_mov_b64_e32 v[132:133], s[52:53]
	v_mov_b64_e32 v[112:113], s[52:53]
	v_mov_b64_e32 v[116:117], s[52:53]
	v_mov_b64_e32 v[96:97], s[52:53]
	v_mov_b64_e32 v[100:101], s[52:53]
	v_mov_b64_e32 v[80:81], s[52:53]
	v_mov_b64_e32 v[84:85], s[52:53]
	s_waitcnt lgkmcnt(0)
	s_nop 3
	v_mfma_f32_16x16x128_f8f6f4 v[128:131], v[20:27], v[8:15], v[128:131]
	s_nop 3
	v_mfma_f32_16x16x128_f8f6f4 v[132:135], v[40:47], v[8:15], v[132:135]
	s_nop 3
	v_mfma_f32_16x16x128_f8f6f4 v[112:115], v[20:27], v[28:35], v[112:115]
	s_nop 3
	v_mfma_f32_16x16x128_f8f6f4 v[116:119], v[40:47], v[28:35], v[116:119]
	s_nop 3
	v_mfma_f32_16x16x128_f8f6f4 v[96:99], v[20:27], v[48:55], v[96:99]
	s_nop 3
	v_mfma_f32_16x16x128_f8f6f4 v[100:103], v[40:47], v[48:55], v[100:103]
	s_nop 3
	v_mfma_f32_16x16x128_f8f6f4 v[80:83], v[20:27], v[56:63], v[80:83]
	s_nop 3
	v_mfma_f32_16x16x128_f8f6f4 v[84:87], v[40:47], v[56:63], v[84:87]
	s_setprio 0
	s_setprio 1
	v_mov_b64_e32 v[122:123], s[54:55]
	v_mov_b64_e32 v[126:127], s[54:55]
	v_mov_b64_e32 v[106:107], s[54:55]
	v_mov_b64_e32 v[110:111], s[54:55]
	v_mov_b64_e32 v[90:91], s[54:55]
	v_mov_b64_e32 v[94:95], s[54:55]
	v_mov_b64_e32 v[74:75], s[54:55]
	v_mov_b64_e32 v[78:79], s[54:55]
	v_mov_b64_e32 v[120:121], s[52:53]
	v_mov_b64_e32 v[124:125], s[52:53]
	v_mov_b64_e32 v[104:105], s[52:53]
	v_mov_b64_e32 v[108:109], s[52:53]
	v_mov_b64_e32 v[88:89], s[52:53]
	v_mov_b64_e32 v[92:93], s[52:53]
	v_mov_b64_e32 v[72:73], s[52:53]
	v_mov_b64_e32 v[76:77], s[52:53]
	s_nop 3
	v_mfma_f32_16x16x128_f8f6f4 v[120:123], v[148:155], v[8:15], v[120:123]
	s_nop 3
	v_mfma_f32_16x16x128_f8f6f4 v[124:127], v[156:163], v[8:15], v[124:127]
	s_nop 3
	v_mfma_f32_16x16x128_f8f6f4 v[104:107], v[148:155], v[28:35], v[104:107]
	s_nop 3
	v_mfma_f32_16x16x128_f8f6f4 v[108:111], v[156:163], v[28:35], v[108:111]
	s_nop 3
	v_mfma_f32_16x16x128_f8f6f4 v[88:91], v[148:155], v[48:55], v[88:91]
	s_nop 3
	v_mfma_f32_16x16x128_f8f6f4 v[92:95], v[156:163], v[48:55], v[92:95]
	s_nop 3
	v_mfma_f32_16x16x128_f8f6f4 v[72:75], v[148:155], v[56:63], v[72:75]
	s_nop 3
	v_mfma_f32_16x16x128_f8f6f4 v[76:79], v[156:163], v[56:63], v[76:79]
	s_setprio 0
	s_barrier
	s_add_i32 s3, s17, s41
	v_lshl_add_u64 v[140:141], s[24:25], 0, v[2:3]
	s_mov_b32 m0, s3
	ds_read_b128 v[164:167], v146 offset:16384
	ds_read_b128 v[168:171], v146 offset:17408
	ds_read_b128 v[172:175], v146 offset:18432
	ds_read_b128 v[176:179], v146 offset:19456
	ds_read_b128 v[180:183], v146 offset:20480
	ds_read_b128 v[184:187], v146 offset:21504
	ds_read_b128 v[188:191], v146 offset:22528
	ds_read_b128 v[192:195], v146 offset:23552
	global_load_lds_dwordx4 v[140:141], off
	v_lshl_add_u64 v[142:143], s[24:25], 0, v[138:139]
	s_add_i32 m0, s3, 0x2000
	s_add_i32 s2, s2, s41
	global_load_lds_dwordx4 v[142:143], off
	v_lshl_add_u64 v[8:9], s[30:31], 0, v[2:3]
	s_mov_b32 m0, s2
	v_lshl_add_u64 v[144:145], s[28:29], 0, v[16:17]
	global_load_lds_dwordx4 v[8:9], off
	v_lshl_add_u64 v[8:9], s[30:31], 0, v[138:139]
	s_add_i32 m0, s2, 0x2000
	v_lshl_add_u64 v[196:197], s[28:29], 0, v[136:137]
	global_load_lds_dwordx4 v[8:9], off
	s_mov_b32 m0, s42
	s_nop 0
	global_load_lds_dwordx4 v[144:145], off
	s_mov_b32 m0, s43
	s_nop 0
	global_load_lds_dwordx4 v[196:197], off
	s_waitcnt vmcnt(8)
	s_waitcnt lgkmcnt(0)
	s_barrier
	s_setprio 1
	v_mov_b64_e32 v[66:67], s[54:55]
	v_mov_b64_e32 v[70:71], s[54:55]
	v_mov_b64_e32 v[48:49], s[52:53]
	v_mov_b64_e32 v[52:53], s[52:53]
	v_mov_b64_e32 v[32:33], s[52:53]
	v_mov_b64_e32 v[36:37], s[52:53]
	v_mov_b64_e32 v[12:13], s[52:53]
	v_mov_b64_e32 v[64:65], s[52:53]
	v_mov_b64_e32 v[68:69], s[52:53]
	v_mov_b64_e32 v[50:51], s[54:55]
	v_mov_b64_e32 v[54:55], s[54:55]
	v_mov_b64_e32 v[34:35], s[54:55]
	v_mov_b64_e32 v[38:39], s[54:55]
	v_mov_b64_e32 v[14:15], s[54:55]
	s_waitcnt lgkmcnt(0)
	s_nop 3
	v_mfma_f32_16x16x128_f8f6f4 v[64:67], v[20:27], v[164:171], v[64:67]
	s_nop 3
	v_mfma_f32_16x16x128_f8f6f4 v[68:71], v[40:47], v[164:171], v[68:71]
	s_nop 3
	v_mfma_f32_16x16x128_f8f6f4 v[48:51], v[20:27], v[172:179], v[48:51]
	s_nop 3
	v_mfma_f32_16x16x128_f8f6f4 v[52:55], v[40:47], v[172:179], v[52:55]
	s_nop 3
	v_mfma_f32_16x16x128_f8f6f4 v[32:35], v[20:27], v[180:187], v[32:35]
	s_nop 3
	v_mfma_f32_16x16x128_f8f6f4 v[36:39], v[40:47], v[180:187], v[36:39]
	s_nop 3
	v_mfma_f32_16x16x128_f8f6f4 v[12:15], v[20:27], v[188:195], v[12:15]
	v_mov_b64_e32 v[20:21], s[52:53]
	v_mov_b64_e32 v[22:23], s[54:55]
	s_nop 3
	v_mfma_f32_16x16x128_f8f6f4 v[20:23], v[40:47], v[188:195], v[20:23]
	s_setprio 0
	s_setprio 1
	v_mov_b64_e32 v[58:59], s[54:55]
	v_mov_b64_e32 v[62:63], s[54:55]
	v_mov_b64_e32 v[40:41], s[52:53]
	v_mov_b64_e32 v[44:45], s[52:53]
	v_mov_b64_e32 v[24:25], s[52:53]
	v_mov_b64_e32 v[28:29], s[52:53]
	v_mov_b64_e32 v[8:9], s[52:53]
	v_mov_b64_e32 v[56:57], s[52:53]
	v_mov_b64_e32 v[60:61], s[52:53]
	v_mov_b64_e32 v[42:43], s[54:55]
	v_mov_b64_e32 v[46:47], s[54:55]
	v_mov_b64_e32 v[26:27], s[54:55]
	v_mov_b64_e32 v[30:31], s[54:55]
	v_mov_b64_e32 v[10:11], s[54:55]
	s_nop 3
	v_mfma_f32_16x16x128_f8f6f4 v[56:59], v[148:155], v[164:171], v[56:59]
	s_nop 3
	v_mfma_f32_16x16x128_f8f6f4 v[60:63], v[156:163], v[164:171], v[60:63]
	s_nop 3
	v_mfma_f32_16x16x128_f8f6f4 v[40:43], v[148:155], v[172:179], v[40:43]
	s_nop 3
	v_mfma_f32_16x16x128_f8f6f4 v[44:47], v[156:163], v[172:179], v[44:47]
	s_nop 3
	v_mfma_f32_16x16x128_f8f6f4 v[24:27], v[148:155], v[180:187], v[24:27]
	s_nop 3
	v_mfma_f32_16x16x128_f8f6f4 v[28:31], v[156:163], v[180:187], v[28:31]
	s_nop 3
	v_mfma_f32_16x16x128_f8f6f4 v[8:11], v[148:155], v[188:195], v[8:11]
	s_nop 3
	v_mfma_f32_16x16x128_f8f6f4 v[4:7], v[156:163], v[188:195], v[4:7]
	s_setprio 0
	s_barrier
	s_add_i32 s2, 0, 0x18000
	v_add_u32_e32 v1, s2, v19
	s_add_i32 s17, 0, 0x1c000
	ds_read_b128 v[148:151], v1
	ds_read_b128 v[152:155], v1 offset:1024
	ds_read_b128 v[156:159], v1 offset:2048
	ds_read_b128 v[160:163], v1 offset:3072
	v_add_u32_e32 v1, s17, v19
	ds_read_b128 v[164:167], v1
	ds_read_b128 v[168:171], v1 offset:1024
	ds_read_b128 v[172:175], v1 offset:2048
	ds_read_b128 v[176:179], v1 offset:3072
	s_mov_b32 m0, s44
	v_lshl_add_u64 v[198:199], s[26:27], 0, v[16:17]
	ds_read_b128 v[180:183], v146 offset:32768
	ds_read_b128 v[184:187], v146 offset:33792
	ds_read_b128 v[188:191], v146 offset:34816
	ds_read_b128 v[192:195], v146 offset:35840
	ds_read_b128 v[204:207], v146 offset:36864
	ds_read_b128 v[208:211], v146 offset:37888
	ds_read_b128 v[230:233], v146 offset:38912
	ds_read_b128 v[234:237], v146 offset:39936
	global_load_lds_dwordx4 v[198:199], off
	v_lshl_add_u64 v[198:199], s[26:27], 0, v[136:137]
	s_mov_b32 m0, s45
	s_nop 0
	global_load_lds_dwordx4 v[198:199], off
	s_waitcnt vmcnt(8)
	s_waitcnt lgkmcnt(0)
	s_barrier
	s_setprio 1
	s_waitcnt lgkmcnt(0)
	s_nop 3
	v_mfma_f32_16x16x128_f8f6f4 v[128:131], v[148:155], v[180:187], v[128:131]
	s_nop 3
	v_mfma_f32_16x16x128_f8f6f4 v[132:135], v[156:163], v[180:187], v[132:135]
	s_nop 3
	v_mfma_f32_16x16x128_f8f6f4 v[112:115], v[148:155], v[188:195], v[112:115]
	s_nop 3
	v_mfma_f32_16x16x128_f8f6f4 v[116:119], v[156:163], v[188:195], v[116:119]
	s_nop 3
	v_mfma_f32_16x16x128_f8f6f4 v[96:99], v[148:155], v[204:211], v[96:99]
	s_nop 3
	v_mfma_f32_16x16x128_f8f6f4 v[100:103], v[156:163], v[204:211], v[100:103]
	s_nop 3
	v_mfma_f32_16x16x128_f8f6f4 v[80:83], v[148:155], v[230:237], v[80:83]
	s_nop 3
	v_mfma_f32_16x16x128_f8f6f4 v[84:87], v[156:163], v[230:237], v[84:87]
	s_setprio 0
	s_setprio 1
	s_nop 3
	v_mfma_f32_16x16x128_f8f6f4 v[120:123], v[164:171], v[180:187], v[120:123]
	s_nop 3
	v_mfma_f32_16x16x128_f8f6f4 v[124:127], v[172:179], v[180:187], v[124:127]
	s_nop 3
	v_mfma_f32_16x16x128_f8f6f4 v[104:107], v[164:171], v[188:195], v[104:107]
	s_nop 3
	v_mfma_f32_16x16x128_f8f6f4 v[108:111], v[172:179], v[188:195], v[108:111]
	s_nop 3
	v_mfma_f32_16x16x128_f8f6f4 v[88:91], v[164:171], v[204:211], v[88:91]
	s_nop 3
	v_mfma_f32_16x16x128_f8f6f4 v[92:95], v[172:179], v[204:211], v[92:95]
	s_nop 3
	v_mfma_f32_16x16x128_f8f6f4 v[72:75], v[164:171], v[230:237], v[72:75]
	s_nop 3
	v_mfma_f32_16x16x128_f8f6f4 v[76:79], v[172:179], v[230:237], v[76:79]
	s_setprio 0
	s_barrier
	s_add_i32 s2, s2, s41
	v_lshl_add_u64 v[140:141], v[140:141], 0, s[86:87]
	s_mov_b32 m0, s2
	ds_read_b128 v[180:183], v146 offset:49152
	ds_read_b128 v[184:187], v146 offset:50176
	ds_read_b128 v[188:191], v146 offset:51200
	ds_read_b128 v[192:195], v146 offset:52224
	ds_read_b128 v[204:207], v146 offset:53248
	ds_read_b128 v[208:211], v146 offset:54272
	ds_read_b128 v[230:233], v146 offset:55296
	ds_read_b128 v[234:237], v146 offset:56320
	global_load_lds_dwordx4 v[140:141], off
	s_add_i32 m0, s2, 0x2000
	s_add_u32 s2, s24, 0x8080
	v_lshl_add_u64 v[140:141], v[142:143], 0, s[86:87]
	s_addc_u32 s3, s25, 0
	s_add_i32 s17, s17, s41
	global_load_lds_dwordx4 v[140:141], off
	v_lshl_add_u64 v[140:141], s[2:3], 0, v[2:3]
	s_mov_b32 m0, s17
	s_nop 0
	global_load_lds_dwordx4 v[140:141], off
	v_lshl_add_u64 v[140:141], s[2:3], 0, v[138:139]
	s_add_i32 m0, s17, 0x2000
	s_nop 0
	global_load_lds_dwordx4 v[140:141], off
	v_lshl_add_u64 v[140:141], v[144:145], 0, s[86:87]
	s_mov_b32 m0, s48
	s_nop 0
	global_load_lds_dwordx4 v[140:141], off
	v_lshl_add_u64 v[140:141], v[196:197], 0, s[86:87]
	s_mov_b32 m0, s49
	s_nop 0
	global_load_lds_dwordx4 v[140:141], off
	s_waitcnt vmcnt(8)
	s_waitcnt lgkmcnt(0)
	s_barrier
	s_setprio 1
	s_waitcnt lgkmcnt(0)
	s_nop 3
	v_mfma_f32_16x16x128_f8f6f4 v[64:67], v[148:155], v[180:187], v[64:67]
	s_nop 3
	v_mfma_f32_16x16x128_f8f6f4 v[68:71], v[156:163], v[180:187], v[68:71]
	s_nop 3
	v_mfma_f32_16x16x128_f8f6f4 v[48:51], v[148:155], v[188:195], v[48:51]
	s_nop 3
	v_mfma_f32_16x16x128_f8f6f4 v[52:55], v[156:163], v[188:195], v[52:55]
	s_nop 3
	v_mfma_f32_16x16x128_f8f6f4 v[32:35], v[148:155], v[204:211], v[32:35]
	s_nop 3
	v_mfma_f32_16x16x128_f8f6f4 v[36:39], v[156:163], v[204:211], v[36:39]
	s_nop 3
	v_mfma_f32_16x16x128_f8f6f4 v[12:15], v[148:155], v[230:237], v[12:15]
	s_nop 3
	v_mfma_f32_16x16x128_f8f6f4 v[20:23], v[156:163], v[230:237], v[20:23]
	s_setprio 0
	s_setprio 1
	s_nop 3
	v_mfma_f32_16x16x128_f8f6f4 v[56:59], v[164:171], v[180:187], v[56:59]
	s_nop 3
	v_mfma_f32_16x16x128_f8f6f4 v[60:63], v[172:179], v[180:187], v[60:63]
	s_nop 3
	v_mfma_f32_16x16x128_f8f6f4 v[40:43], v[164:171], v[188:195], v[40:43]
	s_nop 3
	v_mfma_f32_16x16x128_f8f6f4 v[44:47], v[172:179], v[188:195], v[44:47]
	s_nop 3
	v_mfma_f32_16x16x128_f8f6f4 v[24:27], v[164:171], v[204:211], v[24:27]
	s_nop 3
	v_mfma_f32_16x16x128_f8f6f4 v[28:31], v[172:179], v[204:211], v[28:31]
	s_nop 3
	v_mfma_f32_16x16x128_f8f6f4 v[8:11], v[164:171], v[230:237], v[8:11]
	s_nop 3
	v_mfma_f32_16x16x128_f8f6f4 v[4:7], v[172:179], v[230:237], v[4:7]
	s_setprio 0
	s_barrier
	s_andn2_b64 vcc, exec, s[12:13]
	s_cbranch_vccnz .LBB0_491
	s_barrier

.LBB0_504:
	s_add_u32 s33, s24, s30
	s_addc_u32 s38, s25, s31
	s_add_u32 s34, s33, 0x100
	s_addc_u32 s35, s38, 0
	s_and_b64 s[2:3], s[28:29], exec
	s_cselect_b32 s35, s17, s35
	s_cselect_b32 s34, s60, s34
	s_add_u32 s2, s22, s30
	s_addc_u32 s3, s23, s31
	s_add_u32 s30, s2, 0x100
	s_addc_u32 s31, s3, 0
	s_add_i32 s71, 0, 0x10000
	s_and_b64 s[2:3], s[28:29], exec
	s_cselect_b32 s37, s15, s31
	s_cselect_b32 s36, s61, s30
	s_add_i32 s3, 0, 0x14000
	s_add_u32 s40, s33, 0x20080
	s_addc_u32 s41, s38, 0
	s_add_i32 s70, s71, s48
	s_add_i32 m0, s50, 0xc000
	s_add_i32 s72, s50, 0xe000
	s_add_i32 s65, s70, 0x2000
	v_add_u32_e32 v1, s71, v19
	s_add_u32 s38, s36, 0x10000
	ds_read_b128 v[28:31], v1
	ds_read_b128 v[32:35], v1 offset:1024
	ds_read_b128 v[36:39], v1 offset:2048
	ds_read_b128 v[40:43], v1 offset:3072
	v_add_u32_e32 v1, s3, v19
	s_addc_u32 s39, s37, 0
	s_add_i32 s67, s3, s48
	ds_read_b128 v[4:7], v1
	ds_read_b128 v[8:11], v1 offset:1024
	ds_read_b128 v[20:23], v1 offset:2048
	ds_read_b128 v[24:27], v1 offset:3072
	s_add_i32 s66, s67, 0x2000
	s_add_i32 s64, 0, 0x18000
	s_add_i32 s63, 0, 0x1c000
	s_add_u32 s30, s34, 0x20000
	s_addc_u32 s31, s35, 0
	s_add_i32 s62, s64, s48
	s_add_i32 s2, s62, 0x2000
	s_add_u32 s28, s36, 0x10080
	s_addc_u32 s29, s37, 0
	s_add_i32 s33, s63, s48
	s_add_i32 s3, s33, 0x2000
	v_lshl_add_u64 v[198:199], s[40:41], 0, v[170:171]
	ds_read_b128 v[172:175], v180
	ds_read_b128 v[176:179], v180 offset:1024
	ds_read_b128 v[182:185], v180 offset:2048
	ds_read_b128 v[186:189], v180 offset:3072
	ds_read_b128 v[190:193], v180 offset:4096
	ds_read_b128 v[194:197], v180 offset:5120
	ds_read_b128 v[204:207], v180 offset:6144
	ds_read_b128 v[208:211], v180 offset:7168
	global_load_lds_dwordx4 v[198:199], off
	v_lshl_add_u64 v[198:199], s[40:41], 0, v[168:169]
	s_mov_b32 m0, s72
	s_nop 0
	global_load_lds_dwordx4 v[198:199], off
	s_waitcnt vmcnt(8)
	s_waitcnt lgkmcnt(0)
	s_barrier
	s_setprio 1
	s_waitcnt lgkmcnt(0)
	s_nop 3
	v_mfma_f32_16x16x128_f8f6f4 v[164:167], v[28:35], v[172:179], v[164:167]
	s_nop 3
	v_mfma_f32_16x16x128_f8f6f4 v[160:163], v[36:43], v[172:179], v[160:163]
	s_nop 3
	v_mfma_f32_16x16x128_f8f6f4 v[148:151], v[28:35], v[182:189], v[148:151]
	s_nop 3
	v_mfma_f32_16x16x128_f8f6f4 v[144:147], v[36:43], v[182:189], v[144:147]
	s_nop 3
	v_mfma_f32_16x16x128_f8f6f4 v[132:135], v[28:35], v[190:197], v[132:135]
	s_nop 3
	v_mfma_f32_16x16x128_f8f6f4 v[128:131], v[36:43], v[190:197], v[128:131]
	s_nop 3
	v_mfma_f32_16x16x128_f8f6f4 v[116:119], v[28:35], v[204:211], v[116:119]
	s_nop 3
	v_mfma_f32_16x16x128_f8f6f4 v[112:115], v[36:43], v[204:211], v[112:115]
	s_setprio 0
	s_setprio 1
	s_nop 3
	v_mfma_f32_16x16x128_f8f6f4 v[156:159], v[4:11], v[172:179], v[156:159]
	s_nop 3
	v_mfma_f32_16x16x128_f8f6f4 v[152:155], v[20:27], v[172:179], v[152:155]
	s_nop 3
	v_mfma_f32_16x16x128_f8f6f4 v[140:143], v[4:11], v[182:189], v[140:143]
	s_nop 3
	v_mfma_f32_16x16x128_f8f6f4 v[136:139], v[20:27], v[182:189], v[136:139]
	s_nop 3
	v_mfma_f32_16x16x128_f8f6f4 v[124:127], v[4:11], v[190:197], v[124:127]
	s_nop 3
	v_mfma_f32_16x16x128_f8f6f4 v[120:123], v[20:27], v[190:197], v[120:123]
	s_nop 3
	v_mfma_f32_16x16x128_f8f6f4 v[108:111], v[4:11], v[204:211], v[108:111]
	s_nop 3
	v_mfma_f32_16x16x128_f8f6f4 v[104:107], v[20:27], v[204:211], v[104:107]
	s_setprio 0
	s_barrier
	s_mov_b32 m0, s70
	v_lshl_add_u64 v[172:173], s[36:37], 0, v[2:3]
	ds_read_b128 v[182:185], v180 offset:16384
	ds_read_b128 v[186:189], v180 offset:17408
	ds_read_b128 v[190:193], v180 offset:18432
	ds_read_b128 v[194:197], v180 offset:19456
	ds_read_b128 v[204:207], v180 offset:20480
	ds_read_b128 v[208:211], v180 offset:21504
	ds_read_b128 v[230:233], v180 offset:22528
	ds_read_b128 v[234:237], v180 offset:23552
	global_load_lds_dwordx4 v[172:173], off
	v_lshl_add_u64 v[174:175], s[36:37], 0, v[16:17]
	s_mov_b32 m0, s65
	v_lshl_add_u64 v[176:177], s[38:39], 0, v[2:3]
	global_load_lds_dwordx4 v[174:175], off
	s_mov_b32 m0, s67
	v_lshl_add_u64 v[178:179], s[34:35], 0, v[168:169]
	global_load_lds_dwordx4 v[176:177], off
	v_lshl_add_u64 v[176:177], s[38:39], 0, v[16:17]
	s_mov_b32 m0, s66
	s_nop 0
	global_load_lds_dwordx4 v[176:177], off
	v_lshl_add_u64 v[176:177], s[34:35], 0, v[170:171]
	s_mov_b32 m0, s50
	s_nop 0
	global_load_lds_dwordx4 v[176:177], off
	s_mov_b32 m0, s51
	s_nop 0
	global_load_lds_dwordx4 v[178:179], off
	s_waitcnt vmcnt(8)
	s_waitcnt lgkmcnt(0)
	s_barrier
	s_setprio 1
	s_waitcnt lgkmcnt(0)
	s_nop 3
	v_mfma_f32_16x16x128_f8f6f4 v[100:103], v[28:35], v[182:189], v[100:103]
	s_nop 3
	v_mfma_f32_16x16x128_f8f6f4 v[96:99], v[36:43], v[182:189], v[96:99]
	s_nop 3
	v_mfma_f32_16x16x128_f8f6f4 v[84:87], v[28:35], v[190:197], v[84:87]
	s_nop 3
	v_mfma_f32_16x16x128_f8f6f4 v[80:83], v[36:43], v[190:197], v[80:83]
	s_nop 3
	v_mfma_f32_16x16x128_f8f6f4 v[68:71], v[28:35], v[204:211], v[68:71]
	s_nop 3
	v_mfma_f32_16x16x128_f8f6f4 v[64:67], v[36:43], v[204:211], v[64:67]
	s_nop 3
	v_mfma_f32_16x16x128_f8f6f4 v[52:55], v[28:35], v[230:237], v[52:55]
	s_nop 3
	v_mfma_f32_16x16x128_f8f6f4 v[48:51], v[36:43], v[230:237], v[48:51]
	s_setprio 0
	s_setprio 1
	s_nop 3
	v_mfma_f32_16x16x128_f8f6f4 v[92:95], v[4:11], v[182:189], v[92:95]
	s_nop 3
	v_mfma_f32_16x16x128_f8f6f4 v[88:91], v[20:27], v[182:189], v[88:91]
	s_nop 3
	v_mfma_f32_16x16x128_f8f6f4 v[76:79], v[4:11], v[190:197], v[76:79]
	s_nop 3
	v_mfma_f32_16x16x128_f8f6f4 v[72:75], v[20:27], v[190:197], v[72:75]
	s_nop 3
	v_mfma_f32_16x16x128_f8f6f4 v[60:63], v[4:11], v[204:211], v[60:63]
	s_nop 3
	v_mfma_f32_16x16x128_f8f6f4 v[56:59], v[20:27], v[204:211], v[56:59]
	s_nop 3
	v_mfma_f32_16x16x128_f8f6f4 v[44:47], v[4:11], v[230:237], v[44:47]
	s_nop 3
	v_mfma_f32_16x16x128_f8f6f4 v[12:15], v[20:27], v[230:237], v[12:15]
	s_setprio 0
	s_barrier
	v_add_u32_e32 v1, s64, v19
	ds_read_b128 v[4:7], v1
	ds_read_b128 v[8:11], v1 offset:1024
	ds_read_b128 v[20:23], v1 offset:2048
	ds_read_b128 v[24:27], v1 offset:3072
	v_add_u32_e32 v1, s63, v19
	ds_read_b128 v[28:31], v1
	ds_read_b128 v[32:35], v1 offset:1024
	ds_read_b128 v[36:39], v1 offset:2048
	ds_read_b128 v[40:43], v1 offset:3072
	s_mov_b32 m0, s52
	v_lshl_add_u64 v[198:199], s[30:31], 0, v[170:171]
	ds_read_b128 v[182:185], v180 offset:32768
	ds_read_b128 v[186:189], v180 offset:33792
	ds_read_b128 v[190:193], v180 offset:34816
	ds_read_b128 v[194:197], v180 offset:35840
	ds_read_b128 v[204:207], v180 offset:36864
	ds_read_b128 v[208:211], v180 offset:37888
	ds_read_b128 v[230:233], v180 offset:38912
	ds_read_b128 v[234:237], v180 offset:39936
	global_load_lds_dwordx4 v[198:199], off
	v_lshl_add_u64 v[198:199], s[30:31], 0, v[168:169]
	s_mov_b32 m0, s53
	s_nop 0
	global_load_lds_dwordx4 v[198:199], off
	s_waitcnt vmcnt(8)
	s_waitcnt lgkmcnt(0)
	s_barrier
	s_setprio 1
	s_waitcnt lgkmcnt(0)
	s_nop 3
	v_mfma_f32_16x16x128_f8f6f4 v[164:167], v[4:11], v[182:189], v[164:167]
	s_nop 3
	v_mfma_f32_16x16x128_f8f6f4 v[160:163], v[20:27], v[182:189], v[160:163]
	s_nop 3
	v_mfma_f32_16x16x128_f8f6f4 v[148:151], v[4:11], v[190:197], v[148:151]
	s_nop 3
	v_mfma_f32_16x16x128_f8f6f4 v[144:147], v[20:27], v[190:197], v[144:147]
	s_nop 3
	v_mfma_f32_16x16x128_f8f6f4 v[132:135], v[4:11], v[204:211], v[132:135]
	s_nop 3
	v_mfma_f32_16x16x128_f8f6f4 v[128:131], v[20:27], v[204:211], v[128:131]
	s_nop 3
	v_mfma_f32_16x16x128_f8f6f4 v[116:119], v[4:11], v[230:237], v[116:119]
	s_nop 3
	v_mfma_f32_16x16x128_f8f6f4 v[112:115], v[20:27], v[230:237], v[112:115]
	s_setprio 0
	s_setprio 1
	s_nop 3
	v_mfma_f32_16x16x128_f8f6f4 v[156:159], v[28:35], v[182:189], v[156:159]
	s_nop 3
	v_mfma_f32_16x16x128_f8f6f4 v[152:155], v[36:43], v[182:189], v[152:155]
	s_nop 3
	v_mfma_f32_16x16x128_f8f6f4 v[140:143], v[28:35], v[190:197], v[140:143]
	s_nop 3
	v_mfma_f32_16x16x128_f8f6f4 v[136:139], v[36:43], v[190:197], v[136:139]
	s_nop 3
	v_mfma_f32_16x16x128_f8f6f4 v[124:127], v[28:35], v[204:211], v[124:127]
	s_nop 3
	v_mfma_f32_16x16x128_f8f6f4 v[120:123], v[36:43], v[204:211], v[120:123]
	s_nop 3
	v_mfma_f32_16x16x128_f8f6f4 v[108:111], v[28:35], v[230:237], v[108:111]
	s_nop 3
	v_mfma_f32_16x16x128_f8f6f4 v[104:107], v[36:43], v[230:237], v[104:107]
	s_setprio 0
	s_barrier
	s_mov_b32 m0, s62
	v_lshl_add_u64 v[172:173], v[172:173], 0, s[86:87]
	ds_read_b128 v[182:185], v180 offset:49152
	ds_read_b128 v[186:189], v180 offset:50176
	ds_read_b128 v[190:193], v180 offset:51200
	ds_read_b128 v[194:197], v180 offset:52224
	ds_read_b128 v[204:207], v180 offset:53248
	ds_read_b128 v[208:211], v180 offset:54272
	ds_read_b128 v[230:233], v180 offset:55296
	ds_read_b128 v[234:237], v180 offset:56320
	global_load_lds_dwordx4 v[172:173], off
	v_lshl_add_u64 v[172:173], v[174:175], 0, s[86:87]
	s_mov_b32 m0, s2
	s_nop 0
	global_load_lds_dwordx4 v[172:173], off
	v_lshl_add_u64 v[172:173], s[28:29], 0, v[2:3]
	s_mov_b32 m0, s33
	s_nop 0
	global_load_lds_dwordx4 v[172:173], off
	v_lshl_add_u64 v[172:173], s[28:29], 0, v[16:17]
	s_mov_b32 m0, s3
	s_nop 0
	global_load_lds_dwordx4 v[172:173], off
	v_lshl_add_u64 v[172:173], v[176:177], 0, s[86:87]
	s_mov_b32 m0, s56
	s_nop 0
	global_load_lds_dwordx4 v[172:173], off
	v_lshl_add_u64 v[172:173], v[178:179], 0, s[86:87]
	s_mov_b32 m0, s57
	s_nop 0
	global_load_lds_dwordx4 v[172:173], off
	s_waitcnt vmcnt(8)
	s_waitcnt lgkmcnt(0)
	s_barrier
	s_setprio 1
	s_waitcnt lgkmcnt(0)
	s_nop 3
	v_mfma_f32_16x16x128_f8f6f4 v[100:103], v[4:11], v[182:189], v[100:103]
	s_nop 3
	v_mfma_f32_16x16x128_f8f6f4 v[96:99], v[20:27], v[182:189], v[96:99]
	s_nop 3
	v_mfma_f32_16x16x128_f8f6f4 v[84:87], v[4:11], v[190:197], v[84:87]
	s_nop 3
	v_mfma_f32_16x16x128_f8f6f4 v[80:83], v[20:27], v[190:197], v[80:83]
	s_nop 3
	v_mfma_f32_16x16x128_f8f6f4 v[68:71], v[4:11], v[204:211], v[68:71]
	s_nop 3
	v_mfma_f32_16x16x128_f8f6f4 v[64:67], v[20:27], v[204:211], v[64:67]
	s_nop 3
	v_mfma_f32_16x16x128_f8f6f4 v[52:55], v[4:11], v[230:237], v[52:55]
	s_nop 3
	v_mfma_f32_16x16x128_f8f6f4 v[48:51], v[20:27], v[230:237], v[48:51]
	s_setprio 0
	s_setprio 1
	s_nop 3
	v_mfma_f32_16x16x128_f8f6f4 v[92:95], v[28:35], v[182:189], v[92:95]
	s_nop 3
	v_mfma_f32_16x16x128_f8f6f4 v[88:91], v[36:43], v[182:189], v[88:91]
	s_nop 3
	v_mfma_f32_16x16x128_f8f6f4 v[76:79], v[28:35], v[190:197], v[76:79]
	s_nop 3
	v_mfma_f32_16x16x128_f8f6f4 v[72:75], v[36:43], v[190:197], v[72:75]
	s_nop 3
	v_mfma_f32_16x16x128_f8f6f4 v[60:63], v[28:35], v[204:211], v[60:63]
	s_nop 3
	v_mfma_f32_16x16x128_f8f6f4 v[56:59], v[36:43], v[204:211], v[56:59]
	s_nop 3
	v_mfma_f32_16x16x128_f8f6f4 v[44:47], v[28:35], v[230:237], v[44:47]
	s_nop 3
	v_mfma_f32_16x16x128_f8f6f4 v[12:15], v[36:43], v[230:237], v[12:15]
	s_setprio 0
	s_barrier
	s_andn2_b64 vcc, exec, s[26:27]
	s_mov_b64 s[28:29], -1
	s_mov_b64 s[26:27], 0
	s_mov_b64 s[30:31], 0x100
	s_cbranch_vccz .LBB0_504
	s_and_b64 vcc, exec, s[12:13]
	s_cbranch_vccz .LBB0_507
	s_barrier

.LBB0_952:
	s_add_u32 s3, s20, 0xfffe0080
	s_addc_u32 s22, s21, -1
	s_add_i32 s2, 0, 0x10000
	s_cmp_eq_u32 s49, 4
	s_cselect_b32 s25, s13, s22
	s_cselect_b32 s24, s45, s3
	v_add_u32_e32 v1, s2, v19
	s_cselect_b32 s23, s11, s48
	s_cselect_b32 s22, s46, s47
	s_add_i32 s3, 0, 0x14000
	ds_read_b128 v[28:31], v1
	ds_read_b128 v[32:35], v1 offset:1024
	ds_read_b128 v[36:39], v1 offset:2048
	ds_read_b128 v[40:43], v1 offset:3072
	v_add_u32_e32 v1, s3, v19
	ds_read_b128 v[4:7], v1
	ds_read_b128 v[8:11], v1 offset:1024
	ds_read_b128 v[20:23], v1 offset:2048
	ds_read_b128 v[24:27], v1 offset:3072
	v_lshl_add_u64 v[198:199], s[20:21], 0, v[168:169]
	s_add_i32 m0, s19, 0xc000
	ds_read_b128 v[172:175], v180
	ds_read_b128 v[176:179], v180 offset:1024
	ds_read_b128 v[182:185], v180 offset:2048
	ds_read_b128 v[186:189], v180 offset:3072
	ds_read_b128 v[190:193], v180 offset:4096
	ds_read_b128 v[194:197], v180 offset:5120
	ds_read_b128 v[204:207], v180 offset:6144
	ds_read_b128 v[208:211], v180 offset:7168
	global_load_lds_dwordx4 v[198:199], off
	v_lshl_add_u64 v[198:199], s[20:21], 0, v[170:171]
	s_add_i32 m0, s19, 0xe000
	s_nop 0
	global_load_lds_dwordx4 v[198:199], off
	s_waitcnt vmcnt(8)
	s_waitcnt lgkmcnt(0)
	s_barrier
	s_setprio 1
	s_waitcnt lgkmcnt(0)
	s_nop 3
	v_mfma_f32_16x16x128_f8f6f4 v[164:167], v[28:35], v[172:179], v[164:167]
	s_nop 3
	v_mfma_f32_16x16x128_f8f6f4 v[160:163], v[36:43], v[172:179], v[160:163]
	s_nop 3
	v_mfma_f32_16x16x128_f8f6f4 v[152:155], v[28:35], v[182:189], v[152:155]
	s_nop 3
	v_mfma_f32_16x16x128_f8f6f4 v[144:147], v[36:43], v[182:189], v[144:147]
	s_nop 3
	v_mfma_f32_16x16x128_f8f6f4 v[136:139], v[28:35], v[190:197], v[136:139]
	s_nop 3
	v_mfma_f32_16x16x128_f8f6f4 v[128:131], v[36:43], v[190:197], v[128:131]
	s_nop 3
	v_mfma_f32_16x16x128_f8f6f4 v[120:123], v[28:35], v[204:211], v[120:123]
	s_nop 3
	v_mfma_f32_16x16x128_f8f6f4 v[112:115], v[36:43], v[204:211], v[112:115]
	s_setprio 0
	s_setprio 1
	s_nop 3
	v_mfma_f32_16x16x128_f8f6f4 v[156:159], v[4:11], v[172:179], v[156:159]
	s_nop 3
	v_mfma_f32_16x16x128_f8f6f4 v[148:151], v[20:27], v[172:179], v[148:151]
	s_nop 3
	v_mfma_f32_16x16x128_f8f6f4 v[140:143], v[4:11], v[182:189], v[140:143]
	s_nop 3
	v_mfma_f32_16x16x128_f8f6f4 v[132:135], v[20:27], v[182:189], v[132:135]
	s_nop 3
	v_mfma_f32_16x16x128_f8f6f4 v[124:127], v[4:11], v[190:197], v[124:127]
	s_nop 3
	v_mfma_f32_16x16x128_f8f6f4 v[116:119], v[20:27], v[190:197], v[116:119]
	s_nop 3
	v_mfma_f32_16x16x128_f8f6f4 v[108:111], v[4:11], v[204:211], v[108:111]
	s_nop 3
	v_mfma_f32_16x16x128_f8f6f4 v[104:107], v[20:27], v[204:211], v[104:107]
	s_setprio 0
	s_barrier
	s_add_i32 s2, s2, s35
	v_lshl_add_u64 v[172:173], s[22:23], 0, v[2:3]
	s_mov_b32 m0, s2
	ds_read_b128 v[182:185], v180 offset:16384
	ds_read_b128 v[186:189], v180 offset:17408
	ds_read_b128 v[190:193], v180 offset:18432
	ds_read_b128 v[194:197], v180 offset:19456
	ds_read_b128 v[204:207], v180 offset:20480
	ds_read_b128 v[208:211], v180 offset:21504
	ds_read_b128 v[230:233], v180 offset:22528
	ds_read_b128 v[234:237], v180 offset:23552
	global_load_lds_dwordx4 v[172:173], off
	s_add_i32 m0, s2, 0x2000
	s_add_u32 s50, s22, 0x20000
	v_lshl_add_u64 v[174:175], s[22:23], 0, v[16:17]
	s_addc_u32 s51, s23, 0
	s_add_i32 s2, s3, s35
	global_load_lds_dwordx4 v[174:175], off
	v_lshl_add_u64 v[176:177], s[50:51], 0, v[2:3]
	s_mov_b32 m0, s2
	v_lshl_add_u64 v[178:179], s[24:25], 0, v[16:17]
	global_load_lds_dwordx4 v[176:177], off
	v_lshl_add_u64 v[176:177], s[50:51], 0, v[16:17]
	s_add_i32 m0, s2, 0x2000
	s_nop 0
	global_load_lds_dwordx4 v[176:177], off
	v_lshl_add_u64 v[176:177], s[24:25], 0, v[2:3]
	s_mov_b32 m0, s19
	s_nop 0
	global_load_lds_dwordx4 v[176:177], off
	s_mov_b32 m0, s36
	s_nop 0
	global_load_lds_dwordx4 v[178:179], off
	s_waitcnt vmcnt(8)
	s_waitcnt lgkmcnt(0)
	s_barrier
	s_setprio 1
	s_waitcnt lgkmcnt(0)
	s_nop 3
	v_mfma_f32_16x16x128_f8f6f4 v[100:103], v[28:35], v[182:189], v[100:103]
	s_nop 3
	v_mfma_f32_16x16x128_f8f6f4 v[96:99], v[36:43], v[182:189], v[96:99]
	s_nop 3
	v_mfma_f32_16x16x128_f8f6f4 v[88:91], v[28:35], v[190:197], v[88:91]
	s_nop 3
	v_mfma_f32_16x16x128_f8f6f4 v[80:83], v[36:43], v[190:197], v[80:83]
	s_nop 3
	v_mfma_f32_16x16x128_f8f6f4 v[72:75], v[28:35], v[204:211], v[72:75]
	s_nop 3
	v_mfma_f32_16x16x128_f8f6f4 v[64:67], v[36:43], v[204:211], v[64:67]
	s_nop 3
	v_mfma_f32_16x16x128_f8f6f4 v[56:59], v[28:35], v[230:237], v[56:59]
	s_nop 3
	v_mfma_f32_16x16x128_f8f6f4 v[48:51], v[36:43], v[230:237], v[48:51]
	s_setprio 0
	s_setprio 1
	s_nop 3
	v_mfma_f32_16x16x128_f8f6f4 v[92:95], v[4:11], v[182:189], v[92:95]
	s_nop 3
	v_mfma_f32_16x16x128_f8f6f4 v[84:87], v[20:27], v[182:189], v[84:87]
	s_nop 3
	v_mfma_f32_16x16x128_f8f6f4 v[76:79], v[4:11], v[190:197], v[76:79]
	s_nop 3
	v_mfma_f32_16x16x128_f8f6f4 v[68:71], v[20:27], v[190:197], v[68:71]
	s_nop 3
	v_mfma_f32_16x16x128_f8f6f4 v[60:63], v[4:11], v[204:211], v[60:63]
	s_nop 3
	v_mfma_f32_16x16x128_f8f6f4 v[52:55], v[20:27], v[204:211], v[52:55]
	s_nop 3
	v_mfma_f32_16x16x128_f8f6f4 v[44:47], v[4:11], v[230:237], v[44:47]
	s_nop 3
	v_mfma_f32_16x16x128_f8f6f4 v[12:15], v[20:27], v[230:237], v[12:15]
	s_setprio 0
	s_barrier
	s_add_i32 s33, 0, 0x18000
	v_add_u32_e32 v1, s33, v19
	s_add_i32 s50, 0, 0x1c000
	ds_read_b128 v[4:7], v1
	ds_read_b128 v[8:11], v1 offset:1024
	ds_read_b128 v[20:23], v1 offset:2048
	ds_read_b128 v[24:27], v1 offset:3072
	v_add_u32_e32 v1, s50, v19
	ds_read_b128 v[28:31], v1
	ds_read_b128 v[32:35], v1 offset:1024
	ds_read_b128 v[36:39], v1 offset:2048
	ds_read_b128 v[40:43], v1 offset:3072
	s_add_u32 s2, s24, 0x20000
	s_addc_u32 s3, s25, 0
	s_mov_b32 m0, s37
	v_lshl_add_u64 v[198:199], s[2:3], 0, v[2:3]
	ds_read_b128 v[182:185], v180 offset:32768
	ds_read_b128 v[186:189], v180 offset:33792
	ds_read_b128 v[190:193], v180 offset:34816
	ds_read_b128 v[194:197], v180 offset:35840
	ds_read_b128 v[204:207], v180 offset:36864
	ds_read_b128 v[208:211], v180 offset:37888
	ds_read_b128 v[230:233], v180 offset:38912
	ds_read_b128 v[234:237], v180 offset:39936
	global_load_lds_dwordx4 v[198:199], off
	v_lshl_add_u64 v[198:199], s[2:3], 0, v[16:17]
	s_mov_b32 m0, s38
	s_nop 0
	global_load_lds_dwordx4 v[198:199], off
	s_waitcnt vmcnt(8)
	s_waitcnt lgkmcnt(0)
	s_barrier
	s_setprio 1
	s_waitcnt lgkmcnt(0)
	s_nop 3
	v_mfma_f32_16x16x128_f8f6f4 v[164:167], v[4:11], v[182:189], v[164:167]
	s_nop 3
	v_mfma_f32_16x16x128_f8f6f4 v[160:163], v[20:27], v[182:189], v[160:163]
	s_nop 3
	v_mfma_f32_16x16x128_f8f6f4 v[152:155], v[4:11], v[190:197], v[152:155]
	s_nop 3
	v_mfma_f32_16x16x128_f8f6f4 v[144:147], v[20:27], v[190:197], v[144:147]
	s_nop 3
	v_mfma_f32_16x16x128_f8f6f4 v[136:139], v[4:11], v[204:211], v[136:139]
	s_nop 3
	v_mfma_f32_16x16x128_f8f6f4 v[128:131], v[20:27], v[204:211], v[128:131]
	s_nop 3
	v_mfma_f32_16x16x128_f8f6f4 v[120:123], v[4:11], v[230:237], v[120:123]
	s_nop 3
	v_mfma_f32_16x16x128_f8f6f4 v[112:115], v[20:27], v[230:237], v[112:115]
	s_setprio 0
	s_setprio 1
	s_nop 3
	v_mfma_f32_16x16x128_f8f6f4 v[156:159], v[28:35], v[182:189], v[156:159]
	s_nop 3
	v_mfma_f32_16x16x128_f8f6f4 v[148:151], v[36:43], v[182:189], v[148:151]
	s_nop 3
	v_mfma_f32_16x16x128_f8f6f4 v[140:143], v[28:35], v[190:197], v[140:143]
	s_nop 3
	v_mfma_f32_16x16x128_f8f6f4 v[132:135], v[36:43], v[190:197], v[132:135]
	s_nop 3
	v_mfma_f32_16x16x128_f8f6f4 v[124:127], v[28:35], v[204:211], v[124:127]
	s_nop 3
	v_mfma_f32_16x16x128_f8f6f4 v[116:119], v[36:43], v[204:211], v[116:119]
	s_nop 3
	v_mfma_f32_16x16x128_f8f6f4 v[108:111], v[28:35], v[230:237], v[108:111]
	s_nop 3
	v_mfma_f32_16x16x128_f8f6f4 v[104:107], v[36:43], v[230:237], v[104:107]
	s_setprio 0
	s_barrier
	s_add_i32 s2, s33, s35
	v_lshl_add_u64 v[172:173], v[172:173], 0, s[86:87]
	s_mov_b32 m0, s2
	ds_read_b128 v[182:185], v180 offset:49152
	ds_read_b128 v[186:189], v180 offset:50176
	ds_read_b128 v[190:193], v180 offset:51200
	ds_read_b128 v[194:197], v180 offset:52224
	ds_read_b128 v[204:207], v180 offset:53248
	ds_read_b128 v[208:211], v180 offset:54272
	ds_read_b128 v[230:233], v180 offset:55296
	ds_read_b128 v[234:237], v180 offset:56320
	global_load_lds_dwordx4 v[172:173], off
	s_add_i32 m0, s2, 0x2000
	s_add_u32 s2, s22, 0x20080
	v_lshl_add_u64 v[172:173], v[174:175], 0, s[86:87]
	s_addc_u32 s3, s23, 0
	s_add_i32 s22, s50, s35
	global_load_lds_dwordx4 v[172:173], off
	v_lshl_add_u64 v[172:173], s[2:3], 0, v[2:3]
	s_mov_b32 m0, s22
	s_nop 0
	global_load_lds_dwordx4 v[172:173], off
	v_lshl_add_u64 v[172:173], s[2:3], 0, v[16:17]
	s_add_i32 m0, s22, 0x2000
	s_nop 0
	global_load_lds_dwordx4 v[172:173], off
	v_lshl_add_u64 v[172:173], v[176:177], 0, s[86:87]
	s_mov_b32 m0, s40
	s_nop 0
	global_load_lds_dwordx4 v[172:173], off
	v_lshl_add_u64 v[172:173], v[178:179], 0, s[86:87]
	s_mov_b32 m0, s41
	s_nop 0
	global_load_lds_dwordx4 v[172:173], off
	s_waitcnt vmcnt(8)
	s_waitcnt lgkmcnt(0)
	s_barrier
	s_setprio 1
	s_waitcnt lgkmcnt(0)
	s_nop 3
	v_mfma_f32_16x16x128_f8f6f4 v[100:103], v[4:11], v[182:189], v[100:103]
	s_nop 3
	v_mfma_f32_16x16x128_f8f6f4 v[96:99], v[20:27], v[182:189], v[96:99]
	s_nop 3
	v_mfma_f32_16x16x128_f8f6f4 v[88:91], v[4:11], v[190:197], v[88:91]
	s_nop 3
	v_mfma_f32_16x16x128_f8f6f4 v[80:83], v[20:27], v[190:197], v[80:83]
	s_nop 3
	v_mfma_f32_16x16x128_f8f6f4 v[72:75], v[4:11], v[204:211], v[72:75]
	s_nop 3
	v_mfma_f32_16x16x128_f8f6f4 v[64:67], v[20:27], v[204:211], v[64:67]
	s_nop 3
	v_mfma_f32_16x16x128_f8f6f4 v[56:59], v[4:11], v[230:237], v[56:59]
	s_nop 3
	v_mfma_f32_16x16x128_f8f6f4 v[48:51], v[20:27], v[230:237], v[48:51]
	s_setprio 0
	s_setprio 1
	s_nop 3
	v_mfma_f32_16x16x128_f8f6f4 v[92:95], v[28:35], v[182:189], v[92:95]
	s_nop 3
	v_mfma_f32_16x16x128_f8f6f4 v[84:87], v[36:43], v[182:189], v[84:87]
	s_nop 3
	v_mfma_f32_16x16x128_f8f6f4 v[76:79], v[28:35], v[190:197], v[76:79]
	s_nop 3
	v_mfma_f32_16x16x128_f8f6f4 v[68:71], v[36:43], v[190:197], v[68:71]
	s_nop 3
	v_mfma_f32_16x16x128_f8f6f4 v[60:63], v[28:35], v[204:211], v[60:63]
	s_nop 3
	v_mfma_f32_16x16x128_f8f6f4 v[52:55], v[36:43], v[204:211], v[52:55]
	s_nop 3
	v_mfma_f32_16x16x128_f8f6f4 v[44:47], v[28:35], v[230:237], v[44:47]
	s_nop 3
	v_mfma_f32_16x16x128_f8f6f4 v[12:15], v[36:43], v[230:237], v[12:15]
	s_setprio 0
	s_barrier
	s_add_i32 s49, s49, 2
	s_add_u32 s20, s20, 0x100
	s_addc_u32 s21, s21, 0
	s_add_u32 s47, s47, 0x100
	s_addc_u32 s48, s48, 0
	s_cmp_gt_u32 s49, 5
	s_cbranch_scc0 .LBB0_952
	s_and_b64 vcc, exec, s[8:9]
	s_cbranch_vccz .LBB0_955
	s_barrier

.LBB0_1055:
	s_add_u32 s3, s8, 0xfffe0080
	s_addc_u32 s33, s9, -1
	s_add_i32 s2, 0, 0x10000
	s_cmp_eq_u32 s57, 4
	s_cselect_b32 s37, s1, s33
	s_cselect_b32 s36, s21, s3
	v_add_u32_e32 v1, s2, v19
	s_cselect_b32 s35, s23, s56
	s_cselect_b32 s34, s25, s55
	s_add_i32 s3, 0, 0x14000
	ds_read_b128 v[28:31], v1
	ds_read_b128 v[32:35], v1 offset:1024
	ds_read_b128 v[36:39], v1 offset:2048
	ds_read_b128 v[40:43], v1 offset:3072
	v_add_u32_e32 v1, s3, v19
	ds_read_b128 v[4:7], v1
	ds_read_b128 v[8:11], v1 offset:1024
	ds_read_b128 v[20:23], v1 offset:2048
	ds_read_b128 v[24:27], v1 offset:3072
	v_lshl_add_u64 v[200:201], s[8:9], 0, v[170:171]
	s_add_i32 m0, s31, 0xc000
	ds_read_b128 v[174:177], v182
	ds_read_b128 v[178:181], v182 offset:1024
	ds_read_b128 v[184:187], v182 offset:2048
	ds_read_b128 v[188:191], v182 offset:3072
	ds_read_b128 v[192:195], v182 offset:4096
	ds_read_b128 v[196:199], v182 offset:5120
	ds_read_b128 v[204:207], v182 offset:6144
	ds_read_b128 v[208:211], v182 offset:7168
	global_load_lds_dwordx4 v[200:201], off
	v_lshl_add_u64 v[200:201], s[8:9], 0, v[172:173]
	s_add_i32 m0, s31, 0xe000
	s_nop 0
	global_load_lds_dwordx4 v[200:201], off
	s_waitcnt vmcnt(8)
	s_waitcnt lgkmcnt(0)
	s_barrier
	s_setprio 1
	s_waitcnt lgkmcnt(0)
	s_nop 3
	v_mfma_f32_16x16x128_f8f6f4 v[164:167], v[28:35], v[174:181], v[164:167]
	s_nop 3
	v_mfma_f32_16x16x128_f8f6f4 v[160:163], v[36:43], v[174:181], v[160:163]
	s_nop 3
	v_mfma_f32_16x16x128_f8f6f4 v[148:151], v[28:35], v[184:191], v[148:151]
	s_nop 3
	v_mfma_f32_16x16x128_f8f6f4 v[144:147], v[36:43], v[184:191], v[144:147]
	s_nop 3
	v_mfma_f32_16x16x128_f8f6f4 v[132:135], v[28:35], v[192:199], v[132:135]
	s_nop 3
	v_mfma_f32_16x16x128_f8f6f4 v[128:131], v[36:43], v[192:199], v[128:131]
	s_nop 3
	v_mfma_f32_16x16x128_f8f6f4 v[116:119], v[28:35], v[204:211], v[116:119]
	s_nop 3
	v_mfma_f32_16x16x128_f8f6f4 v[112:115], v[36:43], v[204:211], v[112:115]
	s_setprio 0
	s_setprio 1
	s_nop 3
	v_mfma_f32_16x16x128_f8f6f4 v[156:159], v[4:11], v[174:181], v[156:159]
	s_nop 3
	v_mfma_f32_16x16x128_f8f6f4 v[152:155], v[20:27], v[174:181], v[152:155]
	s_nop 3
	v_mfma_f32_16x16x128_f8f6f4 v[140:143], v[4:11], v[184:191], v[140:143]
	s_nop 3
	v_mfma_f32_16x16x128_f8f6f4 v[136:139], v[20:27], v[184:191], v[136:139]
	s_nop 3
	v_mfma_f32_16x16x128_f8f6f4 v[124:127], v[4:11], v[192:199], v[124:127]
	s_nop 3
	v_mfma_f32_16x16x128_f8f6f4 v[120:123], v[20:27], v[192:199], v[120:123]
	s_nop 3
	v_mfma_f32_16x16x128_f8f6f4 v[108:111], v[4:11], v[204:211], v[108:111]
	s_nop 3
	v_mfma_f32_16x16x128_f8f6f4 v[104:107], v[20:27], v[204:211], v[104:107]
	s_setprio 0
	s_barrier
	s_add_i32 s2, s2, s44
	v_lshl_add_u64 v[174:175], s[34:35], 0, v[16:17]
	s_mov_b32 m0, s2
	ds_read_b128 v[184:187], v182 offset:16384
	ds_read_b128 v[188:191], v182 offset:17408
	ds_read_b128 v[192:195], v182 offset:18432
	ds_read_b128 v[196:199], v182 offset:19456
	ds_read_b128 v[204:207], v182 offset:20480
	ds_read_b128 v[208:211], v182 offset:21504
	ds_read_b128 v[230:233], v182 offset:22528
	ds_read_b128 v[234:237], v182 offset:23552
	global_load_lds_dwordx4 v[174:175], off
	s_add_i32 m0, s2, 0x2000
	s_add_u32 s58, s34, 0x20000
	v_lshl_add_u64 v[176:177], s[34:35], 0, v[168:169]
	s_addc_u32 s59, s35, 0
	s_add_i32 s2, s3, s44
	global_load_lds_dwordx4 v[176:177], off
	v_lshl_add_u64 v[178:179], s[58:59], 0, v[16:17]
	s_mov_b32 m0, s2
	v_lshl_add_u64 v[180:181], s[36:37], 0, v[168:169]
	global_load_lds_dwordx4 v[178:179], off
	v_lshl_add_u64 v[178:179], s[58:59], 0, v[168:169]
	s_add_i32 m0, s2, 0x2000
	s_nop 0
	global_load_lds_dwordx4 v[178:179], off
	v_lshl_add_u64 v[178:179], s[36:37], 0, v[16:17]
	s_mov_b32 m0, s31
	s_nop 0
	global_load_lds_dwordx4 v[178:179], off
	s_mov_b32 m0, s45
	s_nop 0
	global_load_lds_dwordx4 v[180:181], off
	s_waitcnt vmcnt(8)
	s_waitcnt lgkmcnt(0)
	s_barrier
	s_setprio 1
	s_waitcnt lgkmcnt(0)
	s_nop 3
	v_mfma_f32_16x16x128_f8f6f4 v[100:103], v[28:35], v[184:191], v[100:103]
	s_nop 3
	v_mfma_f32_16x16x128_f8f6f4 v[96:99], v[36:43], v[184:191], v[96:99]
	s_nop 3
	v_mfma_f32_16x16x128_f8f6f4 v[84:87], v[28:35], v[192:199], v[84:87]
	s_nop 3
	v_mfma_f32_16x16x128_f8f6f4 v[80:83], v[36:43], v[192:199], v[80:83]
	s_nop 3
	v_mfma_f32_16x16x128_f8f6f4 v[68:71], v[28:35], v[204:211], v[68:71]
	s_nop 3
	v_mfma_f32_16x16x128_f8f6f4 v[64:67], v[36:43], v[204:211], v[64:67]
	s_nop 3
	v_mfma_f32_16x16x128_f8f6f4 v[52:55], v[28:35], v[230:237], v[52:55]
	s_nop 3
	v_mfma_f32_16x16x128_f8f6f4 v[48:51], v[36:43], v[230:237], v[48:51]
	s_setprio 0
	s_setprio 1
	s_nop 3
	v_mfma_f32_16x16x128_f8f6f4 v[92:95], v[4:11], v[184:191], v[92:95]
	s_nop 3
	v_mfma_f32_16x16x128_f8f6f4 v[88:91], v[20:27], v[184:191], v[88:91]
	s_nop 3
	v_mfma_f32_16x16x128_f8f6f4 v[76:79], v[4:11], v[192:199], v[76:79]
	s_nop 3
	v_mfma_f32_16x16x128_f8f6f4 v[72:75], v[20:27], v[192:199], v[72:75]
	s_nop 3
	v_mfma_f32_16x16x128_f8f6f4 v[60:63], v[4:11], v[204:211], v[60:63]
	s_nop 3
	v_mfma_f32_16x16x128_f8f6f4 v[56:59], v[20:27], v[204:211], v[56:59]
	s_nop 3
	v_mfma_f32_16x16x128_f8f6f4 v[44:47], v[4:11], v[230:237], v[44:47]
	s_nop 3
	v_mfma_f32_16x16x128_f8f6f4 v[12:15], v[20:27], v[230:237], v[12:15]
	s_setprio 0
	s_barrier
	s_add_i32 s33, 0, 0x18000
	v_add_u32_e32 v1, s33, v19
	s_add_i32 s58, 0, 0x1c000
	ds_read_b128 v[4:7], v1
	ds_read_b128 v[8:11], v1 offset:1024
	ds_read_b128 v[20:23], v1 offset:2048
	ds_read_b128 v[24:27], v1 offset:3072
	v_add_u32_e32 v1, s58, v19
	ds_read_b128 v[28:31], v1
	ds_read_b128 v[32:35], v1 offset:1024
	ds_read_b128 v[36:39], v1 offset:2048
	ds_read_b128 v[40:43], v1 offset:3072
	s_add_u32 s2, s36, 0x20000
	s_addc_u32 s3, s37, 0
	s_mov_b32 m0, s46
	v_lshl_add_u64 v[200:201], s[2:3], 0, v[16:17]
	ds_read_b128 v[184:187], v182 offset:32768
	ds_read_b128 v[188:191], v182 offset:33792
	ds_read_b128 v[192:195], v182 offset:34816
	ds_read_b128 v[196:199], v182 offset:35840
	ds_read_b128 v[204:207], v182 offset:36864
	ds_read_b128 v[208:211], v182 offset:37888
	ds_read_b128 v[230:233], v182 offset:38912
	ds_read_b128 v[234:237], v182 offset:39936
	global_load_lds_dwordx4 v[200:201], off
	v_lshl_add_u64 v[200:201], s[2:3], 0, v[168:169]
	s_mov_b32 m0, s47
	s_nop 0
	global_load_lds_dwordx4 v[200:201], off
	s_waitcnt vmcnt(8)
	s_waitcnt lgkmcnt(0)
	s_barrier
	s_setprio 1
	s_waitcnt lgkmcnt(0)
	s_nop 3
	v_mfma_f32_16x16x128_f8f6f4 v[164:167], v[4:11], v[184:191], v[164:167]
	s_nop 3
	v_mfma_f32_16x16x128_f8f6f4 v[160:163], v[20:27], v[184:191], v[160:163]
	s_nop 3
	v_mfma_f32_16x16x128_f8f6f4 v[148:151], v[4:11], v[192:199], v[148:151]
	s_nop 3
	v_mfma_f32_16x16x128_f8f6f4 v[144:147], v[20:27], v[192:199], v[144:147]
	s_nop 3
	v_mfma_f32_16x16x128_f8f6f4 v[132:135], v[4:11], v[204:211], v[132:135]
	s_nop 3
	v_mfma_f32_16x16x128_f8f6f4 v[128:131], v[20:27], v[204:211], v[128:131]
	s_nop 3
	v_mfma_f32_16x16x128_f8f6f4 v[116:119], v[4:11], v[230:237], v[116:119]
	s_nop 3
	v_mfma_f32_16x16x128_f8f6f4 v[112:115], v[20:27], v[230:237], v[112:115]
	s_setprio 0
	s_setprio 1
	s_nop 3
	v_mfma_f32_16x16x128_f8f6f4 v[156:159], v[28:35], v[184:191], v[156:159]
	s_nop 3
	v_mfma_f32_16x16x128_f8f6f4 v[152:155], v[36:43], v[184:191], v[152:155]
	s_nop 3
	v_mfma_f32_16x16x128_f8f6f4 v[140:143], v[28:35], v[192:199], v[140:143]
	s_nop 3
	v_mfma_f32_16x16x128_f8f6f4 v[136:139], v[36:43], v[192:199], v[136:139]
	s_nop 3
	v_mfma_f32_16x16x128_f8f6f4 v[124:127], v[28:35], v[204:211], v[124:127]
	s_nop 3
	v_mfma_f32_16x16x128_f8f6f4 v[120:123], v[36:43], v[204:211], v[120:123]
	s_nop 3
	v_mfma_f32_16x16x128_f8f6f4 v[108:111], v[28:35], v[230:237], v[108:111]
	s_nop 3
	v_mfma_f32_16x16x128_f8f6f4 v[104:107], v[36:43], v[230:237], v[104:107]
	s_setprio 0
	s_barrier
	s_add_i32 s2, s33, s44
	v_lshl_add_u64 v[174:175], v[174:175], 0, s[86:87]
	s_mov_b32 m0, s2
	ds_read_b128 v[184:187], v182 offset:49152
	ds_read_b128 v[188:191], v182 offset:50176
	ds_read_b128 v[192:195], v182 offset:51200
	ds_read_b128 v[196:199], v182 offset:52224
	ds_read_b128 v[204:207], v182 offset:53248
	ds_read_b128 v[208:211], v182 offset:54272
	ds_read_b128 v[230:233], v182 offset:55296
	ds_read_b128 v[234:237], v182 offset:56320
	global_load_lds_dwordx4 v[174:175], off
	s_add_i32 m0, s2, 0x2000
	s_add_u32 s2, s34, 0x20080
	v_lshl_add_u64 v[174:175], v[176:177], 0, s[86:87]
	s_addc_u32 s3, s35, 0
	s_add_i32 s33, s58, s44
	global_load_lds_dwordx4 v[174:175], off
	v_lshl_add_u64 v[174:175], s[2:3], 0, v[16:17]
	s_mov_b32 m0, s33
	s_nop 0
	global_load_lds_dwordx4 v[174:175], off
	v_lshl_add_u64 v[174:175], s[2:3], 0, v[168:169]
	s_add_i32 m0, s33, 0x2000
	s_nop 0
	global_load_lds_dwordx4 v[174:175], off
	v_lshl_add_u64 v[174:175], v[178:179], 0, s[86:87]
	s_mov_b32 m0, s50
	s_nop 0
	global_load_lds_dwordx4 v[174:175], off
	v_lshl_add_u64 v[174:175], v[180:181], 0, s[86:87]
	s_mov_b32 m0, s51
	s_nop 0
	global_load_lds_dwordx4 v[174:175], off
	s_waitcnt vmcnt(8)
	s_waitcnt lgkmcnt(0)
	s_barrier
	s_setprio 1
	s_waitcnt lgkmcnt(0)
	s_nop 3
	v_mfma_f32_16x16x128_f8f6f4 v[100:103], v[4:11], v[184:191], v[100:103]
	s_nop 3
	v_mfma_f32_16x16x128_f8f6f4 v[96:99], v[20:27], v[184:191], v[96:99]
	s_nop 3
	v_mfma_f32_16x16x128_f8f6f4 v[84:87], v[4:11], v[192:199], v[84:87]
	s_nop 3
	v_mfma_f32_16x16x128_f8f6f4 v[80:83], v[20:27], v[192:199], v[80:83]
	s_nop 3
	v_mfma_f32_16x16x128_f8f6f4 v[68:71], v[4:11], v[204:211], v[68:71]
	s_nop 3
	v_mfma_f32_16x16x128_f8f6f4 v[64:67], v[20:27], v[204:211], v[64:67]
	s_nop 3
	v_mfma_f32_16x16x128_f8f6f4 v[52:55], v[4:11], v[230:237], v[52:55]
	s_nop 3
	v_mfma_f32_16x16x128_f8f6f4 v[48:51], v[20:27], v[230:237], v[48:51]
	s_setprio 0
	s_setprio 1
	s_nop 3
	v_mfma_f32_16x16x128_f8f6f4 v[92:95], v[28:35], v[184:191], v[92:95]
	s_nop 3
	v_mfma_f32_16x16x128_f8f6f4 v[88:91], v[36:43], v[184:191], v[88:91]
	s_nop 3
	v_mfma_f32_16x16x128_f8f6f4 v[76:79], v[28:35], v[192:199], v[76:79]
	s_nop 3
	v_mfma_f32_16x16x128_f8f6f4 v[72:75], v[36:43], v[192:199], v[72:75]
	s_nop 3
	v_mfma_f32_16x16x128_f8f6f4 v[60:63], v[28:35], v[204:211], v[60:63]
	s_nop 3
	v_mfma_f32_16x16x128_f8f6f4 v[56:59], v[36:43], v[204:211], v[56:59]
	s_nop 3
	v_mfma_f32_16x16x128_f8f6f4 v[44:47], v[28:35], v[230:237], v[44:47]
	s_nop 3
	v_mfma_f32_16x16x128_f8f6f4 v[12:15], v[36:43], v[230:237], v[12:15]
	s_setprio 0
	s_barrier
	s_add_i32 s57, s57, 2
	s_add_u32 s8, s8, 0x100
	s_addc_u32 s9, s9, 0
	s_add_u32 s55, s55, 0x100
	s_addc_u32 s56, s56, 0
	s_cmp_gt_u32 s57, 5
	s_cbranch_scc0 .LBB0_1055
	s_and_b64 vcc, exec, s[16:17]
	s_cbranch_vccz .LBB0_1058
	s_barrier

.LBB0_1931:
	s_add_u32 s3, s50, 0x100
	s_addc_u32 s31, s51, 0
	s_and_b64 s[0:1], s[52:53], exec
	s_cselect_b32 s51, s90, s31
	s_cselect_b32 s50, s91, s3
	s_add_u32 s0, s18, s2
	s_addc_u32 s1, s19, 0
	s_add_u32 s2, s0, 0x100
	s_waitcnt vmcnt(8)
	s_addc_u32 s3, s1, 0
	s_waitcnt lgkmcnt(0)
	s_and_b64 s[0:1], s[52:53], exec
	s_cselect_b32 s0, s92, s2
	s_cselect_b32 s1, s35, s3
	s_barrier
	s_setprio 1
	s_waitcnt lgkmcnt(0)
	s_nop 3
	v_mfma_f32_16x16x128_f8f6f4 v[196:199], v[36:43], v[68:75], v[196:199]
	s_nop 3
	v_mfma_f32_16x16x128_f8f6f4 v[192:195], v[28:35], v[68:75], v[192:195]
	s_nop 3
	v_mfma_f32_16x16x128_f8f6f4 v[188:191], v[36:43], v[60:67], v[188:191]
	s_nop 3
	v_mfma_f32_16x16x128_f8f6f4 v[184:187], v[28:35], v[60:67], v[184:187]
	s_nop 3
	v_mfma_f32_16x16x128_f8f6f4 v[180:183], v[36:43], v[52:59], v[180:183]
	s_nop 3
	v_mfma_f32_16x16x128_f8f6f4 v[176:179], v[28:35], v[52:59], v[176:179]
	s_nop 3
	v_mfma_f32_16x16x128_f8f6f4 v[172:175], v[36:43], v[44:51], v[172:175]
	s_nop 3
	v_mfma_f32_16x16x128_f8f6f4 v[168:171], v[28:35], v[44:51], v[168:171]
	s_setprio 0
	s_setprio 1
	s_nop 3
	v_mfma_f32_16x16x128_f8f6f4 v[164:167], v[20:27], v[68:75], v[164:167]
	s_nop 3
	v_mfma_f32_16x16x128_f8f6f4 v[160:163], v[4:11], v[68:75], v[160:163]
	s_nop 3
	v_mfma_f32_16x16x128_f8f6f4 v[156:159], v[20:27], v[60:67], v[156:159]
	s_nop 3
	v_mfma_f32_16x16x128_f8f6f4 v[152:155], v[4:11], v[60:67], v[152:155]
	s_nop 3
	v_mfma_f32_16x16x128_f8f6f4 v[148:151], v[20:27], v[52:59], v[148:151]
	s_nop 3
	v_mfma_f32_16x16x128_f8f6f4 v[144:147], v[4:11], v[52:59], v[144:147]
	s_nop 3
	v_mfma_f32_16x16x128_f8f6f4 v[140:143], v[20:27], v[44:51], v[140:143]
	s_nop 3
	v_mfma_f32_16x16x128_f8f6f4 v[136:139], v[4:11], v[44:51], v[136:139]
	s_setprio 0
	s_barrier
	s_mov_b32 m0, s64
	v_lshl_add_u64 v[46:47], s[0:1], 0, v[16:17]
	s_add_u32 s2, s0, 0x20000
	ds_read_b128 v[52:55], v244 offset:16384
	ds_read_b128 v[56:59], v244 offset:17408
	ds_read_b128 v[60:63], v244 offset:18432
	ds_read_b128 v[64:67], v244 offset:19456
	ds_read_b128 v[68:71], v244 offset:20480
	ds_read_b128 v[72:75], v244 offset:21504
	ds_read_b128 v[228:231], v244 offset:22528
	ds_read_b128 v[232:235], v244 offset:23552
	global_load_lds_dwordx4 v[46:47], off
	v_lshl_add_u64 v[44:45], s[0:1], 0, v[208:209]
	s_mov_b32 m0, s65
	s_addc_u32 s3, s1, 0
	global_load_lds_dwordx4 v[44:45], off
	v_lshl_add_u64 v[48:49], s[2:3], 0, v[16:17]
	s_mov_b32 m0, s66
	v_mov_b32_e32 v207, v3
	global_load_lds_dwordx4 v[48:49], off
	v_lshl_add_u64 v[48:49], s[2:3], 0, v[208:209]
	s_mov_b32 m0, s67
	v_mov_b32_e32 v205, v3
	global_load_lds_dwordx4 v[48:49], off
	s_mov_b32 m0, s63
	v_lshl_add_u64 v[50:51], s[50:51], 0, v[206:207]
	global_load_lds_dwordx4 v206, s[50:51]
	s_mov_b32 m0, s70
	v_lshl_add_u64 v[48:49], s[50:51], 0, v[204:205]
	global_load_lds_dwordx4 v204, s[50:51]
	s_waitcnt vmcnt(8)
	s_waitcnt lgkmcnt(0)
	s_barrier
	s_setprio 1
	s_waitcnt lgkmcnt(0)
	s_nop 3
	v_mfma_f32_16x16x128_f8f6f4 v[132:135], v[36:43], v[52:59], v[132:135]
	s_nop 3
	v_mfma_f32_16x16x128_f8f6f4 v[128:131], v[28:35], v[52:59], v[128:131]
	s_nop 3
	v_mfma_f32_16x16x128_f8f6f4 v[124:127], v[36:43], v[60:67], v[124:127]
	s_nop 3
	v_mfma_f32_16x16x128_f8f6f4 v[120:123], v[28:35], v[60:67], v[120:123]
	s_nop 3
	v_mfma_f32_16x16x128_f8f6f4 v[116:119], v[36:43], v[68:75], v[116:119]
	s_nop 3
	v_mfma_f32_16x16x128_f8f6f4 v[112:115], v[28:35], v[68:75], v[112:115]
	s_nop 3
	v_mfma_f32_16x16x128_f8f6f4 v[108:111], v[36:43], v[228:235], v[108:111]
	s_nop 3
	v_mfma_f32_16x16x128_f8f6f4 v[104:107], v[28:35], v[228:235], v[104:107]
	s_setprio 0
	s_setprio 1
	s_nop 3
	v_mfma_f32_16x16x128_f8f6f4 v[100:103], v[20:27], v[52:59], v[100:103]
	s_nop 3
	v_mfma_f32_16x16x128_f8f6f4 v[96:99], v[4:11], v[52:59], v[96:99]
	s_nop 3
	v_mfma_f32_16x16x128_f8f6f4 v[92:95], v[20:27], v[60:67], v[92:95]
	s_nop 3
	v_mfma_f32_16x16x128_f8f6f4 v[88:91], v[4:11], v[60:67], v[88:91]
	s_nop 3
	v_mfma_f32_16x16x128_f8f6f4 v[84:87], v[20:27], v[68:75], v[84:87]
	s_nop 3
	v_mfma_f32_16x16x128_f8f6f4 v[80:83], v[4:11], v[68:75], v[80:83]
	s_nop 3
	v_mfma_f32_16x16x128_f8f6f4 v[76:79], v[20:27], v[228:235], v[76:79]
	s_nop 3
	v_mfma_f32_16x16x128_f8f6f4 v[12:15], v[4:11], v[228:235], v[12:15]
	s_setprio 0
	s_barrier
	s_add_i32 s2, 0, 0x18000
	s_add_i32 s3, 0, 0x1c000
	v_add_u32_e32 v24, s2, v239
	v_add_u32_e32 v40, s3, v239
	ds_read_b128 v[4:7], v24
	ds_read_b128 v[8:11], v24 offset:1024
	ds_read_b128 v[20:23], v24 offset:2048
	ds_read_b128 v[24:27], v24 offset:3072
	ds_read_b128 v[28:31], v40
	ds_read_b128 v[32:35], v40 offset:1024
	ds_read_b128 v[36:39], v40 offset:2048
	ds_read_b128 v[40:43], v40 offset:3072
	s_mov_b32 m0, s71
	v_lshl_add_u64 v[200:201], s[50:51], 0, v[2:3]
	ds_read_b128 v[52:55], v244 offset:32768
	ds_read_b128 v[56:59], v244 offset:33792
	ds_read_b128 v[60:63], v244 offset:34816
	ds_read_b128 v[64:67], v244 offset:35840
	ds_read_b128 v[68:71], v244 offset:36864
	ds_read_b128 v[72:75], v244 offset:37888
	ds_read_b128 v[228:231], v244 offset:38912
	ds_read_b128 v[232:235], v244 offset:39936
	global_load_lds_dwordx4 v[200:201], off
	v_lshl_add_u64 v[200:201], s[50:51], 0, v[210:211]
	s_mov_b32 m0, s74
	s_nop 0
	global_load_lds_dwordx4 v[200:201], off
	s_waitcnt vmcnt(8)
	s_waitcnt lgkmcnt(0)
	s_barrier
	s_setprio 1
	s_waitcnt lgkmcnt(0)
	s_nop 3
	v_mfma_f32_16x16x128_f8f6f4 v[196:199], v[4:11], v[52:59], v[196:199]
	s_nop 3
	v_mfma_f32_16x16x128_f8f6f4 v[192:195], v[20:27], v[52:59], v[192:195]
	s_nop 3
	v_mfma_f32_16x16x128_f8f6f4 v[188:191], v[4:11], v[60:67], v[188:191]
	s_nop 3
	v_mfma_f32_16x16x128_f8f6f4 v[184:187], v[20:27], v[60:67], v[184:187]
	s_nop 3
	v_mfma_f32_16x16x128_f8f6f4 v[180:183], v[4:11], v[68:75], v[180:183]
	s_nop 3
	v_mfma_f32_16x16x128_f8f6f4 v[176:179], v[20:27], v[68:75], v[176:179]
	s_nop 3
	v_mfma_f32_16x16x128_f8f6f4 v[172:175], v[4:11], v[228:235], v[172:175]
	s_nop 3
	v_mfma_f32_16x16x128_f8f6f4 v[168:171], v[20:27], v[228:235], v[168:171]
	s_setprio 0
	s_setprio 1
	s_nop 3
	v_mfma_f32_16x16x128_f8f6f4 v[164:167], v[28:35], v[52:59], v[164:167]
	s_nop 3
	v_mfma_f32_16x16x128_f8f6f4 v[160:163], v[36:43], v[52:59], v[160:163]
	s_nop 3
	v_mfma_f32_16x16x128_f8f6f4 v[156:159], v[28:35], v[60:67], v[156:159]
	s_nop 3
	v_mfma_f32_16x16x128_f8f6f4 v[152:155], v[36:43], v[60:67], v[152:155]
	s_nop 3
	v_mfma_f32_16x16x128_f8f6f4 v[148:151], v[28:35], v[68:75], v[148:151]
	s_nop 3
	v_mfma_f32_16x16x128_f8f6f4 v[144:147], v[36:43], v[68:75], v[144:147]
	s_nop 3
	v_mfma_f32_16x16x128_f8f6f4 v[140:143], v[28:35], v[228:235], v[140:143]
	s_nop 3
	v_mfma_f32_16x16x128_f8f6f4 v[136:139], v[36:43], v[228:235], v[136:139]
	s_setprio 0
	s_barrier
	s_mov_b64 s[50:51], 0x80
	s_add_i32 s2, s2, s11
	v_lshl_add_u64 v[46:47], v[46:47], 0, s[50:51]
	s_mov_b32 m0, s2
	ds_read_b128 v[52:55], v244 offset:49152
	ds_read_b128 v[56:59], v244 offset:50176
	ds_read_b128 v[60:63], v244 offset:51200
	ds_read_b128 v[64:67], v244 offset:52224
	ds_read_b128 v[68:71], v244 offset:53248
	ds_read_b128 v[72:75], v244 offset:54272
	ds_read_b128 v[228:231], v244 offset:55296
	ds_read_b128 v[232:235], v244 offset:56320
	global_load_lds_dwordx4 v[46:47], off
	s_add_i32 m0, s2, 0x2000
	s_add_u32 s0, s0, 0x20080
	v_lshl_add_u64 v[44:45], v[44:45], 0, s[50:51]
	s_addc_u32 s1, s1, 0
	s_add_i32 s2, s3, s11
	global_load_lds_dwordx4 v[44:45], off
	v_lshl_add_u64 v[44:45], s[0:1], 0, v[16:17]
	s_mov_b32 m0, s2
	s_nop 0
	global_load_lds_dwordx4 v[44:45], off
	v_lshl_add_u64 v[44:45], s[0:1], 0, v[208:209]
	s_add_i32 m0, s2, 0x2000
	s_nop 0
	global_load_lds_dwordx4 v[44:45], off
	v_lshl_add_u64 v[44:45], v[50:51], 0, s[50:51]
	s_mov_b32 m0, s82
	s_nop 0
	global_load_lds_dwordx4 v[44:45], off
	v_lshl_add_u64 v[44:45], v[48:49], 0, s[50:51]
	s_mov_b32 m0, s83
	s_nop 0
	global_load_lds_dwordx4 v[44:45], off
	s_waitcnt vmcnt(8)
	s_waitcnt lgkmcnt(0)
	s_barrier
	s_setprio 1
	s_waitcnt lgkmcnt(0)
	s_nop 3
	v_mfma_f32_16x16x128_f8f6f4 v[132:135], v[4:11], v[52:59], v[132:135]
	s_nop 3
	v_mfma_f32_16x16x128_f8f6f4 v[128:131], v[20:27], v[52:59], v[128:131]
	s_nop 3
	v_mfma_f32_16x16x128_f8f6f4 v[124:127], v[4:11], v[60:67], v[124:127]
	s_nop 3
	v_mfma_f32_16x16x128_f8f6f4 v[120:123], v[20:27], v[60:67], v[120:123]
	s_nop 3
	v_mfma_f32_16x16x128_f8f6f4 v[116:119], v[4:11], v[68:75], v[116:119]
	s_nop 3
	v_mfma_f32_16x16x128_f8f6f4 v[112:115], v[20:27], v[68:75], v[112:115]
	s_nop 3
	v_mfma_f32_16x16x128_f8f6f4 v[108:111], v[4:11], v[228:235], v[108:111]
	s_nop 3
	v_mfma_f32_16x16x128_f8f6f4 v[104:107], v[20:27], v[228:235], v[104:107]
	s_setprio 0
	s_setprio 1
	s_nop 3
	v_mfma_f32_16x16x128_f8f6f4 v[100:103], v[28:35], v[52:59], v[100:103]
	s_nop 3
	v_mfma_f32_16x16x128_f8f6f4 v[96:99], v[36:43], v[52:59], v[96:99]
	s_nop 3
	v_mfma_f32_16x16x128_f8f6f4 v[92:95], v[28:35], v[60:67], v[92:95]
	s_nop 3
	v_mfma_f32_16x16x128_f8f6f4 v[88:91], v[36:43], v[60:67], v[88:91]
	s_nop 3
	v_mfma_f32_16x16x128_f8f6f4 v[84:87], v[28:35], v[68:75], v[84:87]
	s_nop 3
	v_mfma_f32_16x16x128_f8f6f4 v[80:83], v[36:43], v[68:75], v[80:83]
	s_nop 3
	v_mfma_f32_16x16x128_f8f6f4 v[76:79], v[28:35], v[228:235], v[76:79]
	s_nop 3
	v_mfma_f32_16x16x128_f8f6f4 v[12:15], v[36:43], v[228:235], v[12:15]
	s_setprio 0
	s_barrier
	s_add_i32 s0, s89, 2
	s_cmp_gt_u32 s89, 5
	s_cbranch_scc1 .LBB0_1937
	s_mov_b32 s89, s0
	s_branch .LBB0_1899
